# scan_s3: first four forward row groups loaded before the chunk carry-in loops (HBM busy during the carry phase)
# speedup vs baseline: 1.0035x; 1.0035x over previous
; __device__ __forceinline__ float bf_lo(unsigned w) { return __uint_as_float(w << 16); }
; __device__ __forceinline__ float bf_hi(unsigned w) { return __uint_as_float(w & 0xffff0000u); }
; __device__ __forceinline__ void scan_s3(CTXA) {
;     ...
;         for (int g = 0; g < 4; ++g) { unsigned wl[16], wb[16];
; #pragma unroll
;             for (int q = 0; q < 16; ++q) { const int t = g * 16 + q; wl[q] = __builtin_nontemporal_load(la0 + (size_t)t * (D / 2)); wb[q] = __builtin_nontemporal_load(bb0 + (size_t)t * (D / 2)); }
; #pragma unroll
;             for (int q = 0; q < 16; ++q) { const int t = g * 16 + q; hf0 = __expf(bf_lo(wl[q])) * hf0 + bf_lo(wb[q]); hf1 = __expf(bf_hi(wl[q])) * hf1 + bf_hi(wb[q]); fv0[t] = hf0; fv1[t] = hf1; } }
; #pragma unroll
;         for (int g = 0; g < 4; ++g) { unsigned wl[16], wb[16], wg[16];
; #pragma unroll
;             for (int q = 0; q < 16; ++q) { const int t = 63 - (g * 16 + q); wl[q] = __builtin_nontemporal_load(la1 + (size_t)t * (D / 2)); wb[q] = __builtin_nontemporal_load(bb1 + (size_t)t * (D / 2)); wg[q] = __builtin_nontemporal_load(gg + (size_t)t * (D / 2)); }
.LBB0_173:
	v_mov_b32_e32 v232, v231
	global_load_dwordx4 v[18:21], v231, s[82:83] nt
	global_load_dwordx4 v[22:25], v231, s[84:85] nt
	global_load_dwordx4 v[26:29], v231, s[78:79] nt
	v_add_u32_e32 v231, 0xffffe000, v231
	global_load_dwordx4 v[30:33], v231, s[82:83] nt
	global_load_dwordx4 v[34:37], v231, s[84:85] nt
	global_load_dwordx4 v[38:41], v231, s[78:79] nt
	v_add_u32_e32 v231, 0xffffe000, v231
	global_load_dwordx4 v[42:45], v231, s[82:83] nt
	global_load_dwordx4 v[46:49], v231, s[84:85] nt
	global_load_dwordx4 v[50:53], v231, s[78:79] nt
	v_add_u32_e32 v231, 0xffffe000, v231
	global_load_dwordx4 v[54:57], v231, s[82:83] nt
	global_load_dwordx4 v[58:61], v231, s[84:85] nt
	global_load_dwordx4 v[62:65], v231, s[78:79] nt
	v_add_u32_e32 v231, 0xffffe000, v231
	s_waitcnt vmcnt(18)
	v_permlane16_swap_b32_e32 v198, v199
	v_permlane16_swap_b32_e32 v200, v201
	v_permlane16_swap_b32_e32 v202, v203
	v_permlane16_swap_b32_e32 v204, v205
	v_permlane32_swap_b32_e32 v198, v200
	v_permlane32_swap_b32_e32 v199, v201
	v_permlane32_swap_b32_e32 v202, v204
	v_permlane32_swap_b32_e32 v203, v205
	v_and_b32_e32 v6, 0xffff0000, v198
	v_lshlrev_b32_e32 v198, 16, v198
	v_and_b32_e32 v7, 0xffff0000, v199
	v_lshlrev_b32_e32 v199, 16, v199
	v_and_b32_e32 v14, 0xffff0000, v200
	v_lshlrev_b32_e32 v200, 16, v200
	v_and_b32_e32 v15, 0xffff0000, v201
	v_lshlrev_b32_e32 v201, 16, v201
	v_mul_f32_e32 v198, 0x3fb8aa3b, v198
	v_mul_f32_e32 v6, 0x3fb8aa3b, v6
	v_mul_f32_e32 v199, 0x3fb8aa3b, v199
	v_mul_f32_e32 v7, 0x3fb8aa3b, v7
	v_mul_f32_e32 v200, 0x3fb8aa3b, v200
	v_mul_f32_e32 v14, 0x3fb8aa3b, v14
	v_mul_f32_e32 v201, 0x3fb8aa3b, v201
	v_mul_f32_e32 v15, 0x3fb8aa3b, v15
	v_exp_f32_e32 v198, v198
	v_exp_f32_e32 v6, v6
	v_exp_f32_e32 v199, v199
	v_exp_f32_e32 v7, v7
	v_exp_f32_e32 v200, v200
	v_exp_f32_e32 v14, v14
	v_exp_f32_e32 v201, v201
	v_exp_f32_e32 v15, v15
	v_lshlrev_b32_e32 v68, 16, v202
	v_and_b32_e32 v69, 0xffff0000, v202
	v_fmac_f32_e32 v68, v8, v198
	v_fmac_f32_e32 v69, v9, v6
	v_lshlrev_b32_e32 v70, 16, v203
	v_and_b32_e32 v71, 0xffff0000, v203
	v_fmac_f32_e32 v70, v68, v199
	v_fmac_f32_e32 v71, v69, v7
	v_lshlrev_b32_e32 v72, 16, v204
	v_and_b32_e32 v73, 0xffff0000, v204
	v_fmac_f32_e32 v72, v70, v200
	v_fmac_f32_e32 v73, v71, v14
	v_lshlrev_b32_e32 v74, 16, v205
	v_and_b32_e32 v75, 0xffff0000, v205
	v_fmac_f32_e32 v74, v72, v201
	v_fmac_f32_e32 v75, v73, v15
	global_load_dwordx4 v[198:201], v230, s[70:71] nt
	global_load_dwordx4 v[202:205], v230, s[72:73] nt
	v_add_u32_e32 v230, 0x2000, v230
	s_waitcnt vmcnt(18)
	v_permlane16_swap_b32_e32 v206, v207
	v_permlane16_swap_b32_e32 v208, v209
	v_permlane16_swap_b32_e32 v210, v211
	v_permlane16_swap_b32_e32 v212, v213
	v_permlane32_swap_b32_e32 v206, v208
	v_permlane32_swap_b32_e32 v207, v209
	v_permlane32_swap_b32_e32 v210, v212
	v_permlane32_swap_b32_e32 v211, v213
	v_and_b32_e32 v6, 0xffff0000, v206
	v_lshlrev_b32_e32 v206, 16, v206
	v_and_b32_e32 v7, 0xffff0000, v207
	v_lshlrev_b32_e32 v207, 16, v207
	v_and_b32_e32 v14, 0xffff0000, v208
	v_lshlrev_b32_e32 v208, 16, v208
	v_and_b32_e32 v15, 0xffff0000, v209
	v_lshlrev_b32_e32 v209, 16, v209
	v_mul_f32_e32 v206, 0x3fb8aa3b, v206
	v_mul_f32_e32 v6, 0x3fb8aa3b, v6
	v_mul_f32_e32 v207, 0x3fb8aa3b, v207
	v_mul_f32_e32 v7, 0x3fb8aa3b, v7
	v_mul_f32_e32 v208, 0x3fb8aa3b, v208
	v_mul_f32_e32 v14, 0x3fb8aa3b, v14
	v_mul_f32_e32 v209, 0x3fb8aa3b, v209
	v_mul_f32_e32 v15, 0x3fb8aa3b, v15
	v_exp_f32_e32 v206, v206
	v_exp_f32_e32 v6, v6
	v_exp_f32_e32 v207, v207
	v_exp_f32_e32 v7, v7
	v_exp_f32_e32 v208, v208
	v_exp_f32_e32 v14, v14
	v_exp_f32_e32 v209, v209
	v_exp_f32_e32 v15, v15
	v_lshlrev_b32_e32 v76, 16, v210
	v_and_b32_e32 v77, 0xffff0000, v210
	v_fmac_f32_e32 v76, v74, v206
	v_fmac_f32_e32 v77, v75, v6
	v_lshlrev_b32_e32 v78, 16, v211
	v_and_b32_e32 v79, 0xffff0000, v211
	v_fmac_f32_e32 v78, v76, v207
	v_fmac_f32_e32 v79, v77, v7
	v_lshlrev_b32_e32 v80, 16, v212
	v_and_b32_e32 v81, 0xffff0000, v212
	v_fmac_f32_e32 v80, v78, v208
	v_fmac_f32_e32 v81, v79, v14
	v_lshlrev_b32_e32 v82, 16, v213
	v_and_b32_e32 v83, 0xffff0000, v213
	v_fmac_f32_e32 v82, v80, v209
	v_fmac_f32_e32 v83, v81, v15
	global_load_dwordx4 v[206:209], v230, s[70:71] nt
	global_load_dwordx4 v[210:213], v230, s[72:73] nt
	v_add_u32_e32 v230, 0x2000, v230
	s_waitcnt vmcnt(18)
	v_permlane16_swap_b32_e32 v214, v215
	v_permlane16_swap_b32_e32 v216, v217
	v_permlane16_swap_b32_e32 v218, v219
	v_permlane16_swap_b32_e32 v220, v221
	v_permlane32_swap_b32_e32 v214, v216
	v_permlane32_swap_b32_e32 v215, v217
	v_permlane32_swap_b32_e32 v218, v220
	v_permlane32_swap_b32_e32 v219, v221
	v_and_b32_e32 v6, 0xffff0000, v214
	v_lshlrev_b32_e32 v214, 16, v214
	v_and_b32_e32 v7, 0xffff0000, v215
	v_lshlrev_b32_e32 v215, 16, v215
	v_and_b32_e32 v14, 0xffff0000, v216
	v_lshlrev_b32_e32 v216, 16, v216
	v_and_b32_e32 v15, 0xffff0000, v217
	v_lshlrev_b32_e32 v217, 16, v217
	v_mul_f32_e32 v214, 0x3fb8aa3b, v214
	v_mul_f32_e32 v6, 0x3fb8aa3b, v6
	v_mul_f32_e32 v215, 0x3fb8aa3b, v215
	v_mul_f32_e32 v7, 0x3fb8aa3b, v7
	v_mul_f32_e32 v216, 0x3fb8aa3b, v216
	v_mul_f32_e32 v14, 0x3fb8aa3b, v14
	v_mul_f32_e32 v217, 0x3fb8aa3b, v217
	v_mul_f32_e32 v15, 0x3fb8aa3b, v15
	v_exp_f32_e32 v214, v214
	v_exp_f32_e32 v6, v6
	v_exp_f32_e32 v215, v215
	v_exp_f32_e32 v7, v7
	v_exp_f32_e32 v216, v216
	v_exp_f32_e32 v14, v14
	v_exp_f32_e32 v217, v217
	v_exp_f32_e32 v15, v15
	v_lshlrev_b32_e32 v84, 16, v218
	v_and_b32_e32 v85, 0xffff0000, v218
	v_fmac_f32_e32 v84, v82, v214
	v_fmac_f32_e32 v85, v83, v6
	v_lshlrev_b32_e32 v86, 16, v219
	v_and_b32_e32 v87, 0xffff0000, v219
	v_fmac_f32_e32 v86, v84, v215
	v_fmac_f32_e32 v87, v85, v7
	v_lshlrev_b32_e32 v88, 16, v220
	v_and_b32_e32 v89, 0xffff0000, v220
	v_fmac_f32_e32 v88, v86, v216
	v_fmac_f32_e32 v89, v87, v14
	v_lshlrev_b32_e32 v90, 16, v221
	v_and_b32_e32 v91, 0xffff0000, v221
	v_fmac_f32_e32 v90, v88, v217
	v_fmac_f32_e32 v91, v89, v15
	global_load_dwordx4 v[214:217], v230, s[70:71] nt
	global_load_dwordx4 v[218:221], v230, s[72:73] nt
	v_add_u32_e32 v230, 0x2000, v230
	s_waitcnt vmcnt(18)
; __device__ __forceinline__ float bf_lo(unsigned w) { return __uint_as_float(w << 16); }
; __device__ __forceinline__ float bf_hi(unsigned w) { return __uint_as_float(w & 0xffff0000u); }
; __device__ __forceinline__ void scan_s3(CTXA) {
;     ...
;         for (int g = 0; g < 4; ++g) { unsigned wl[16], wb[16];
; #pragma unroll
;             for (int q = 0; q < 16; ++q) { const int t = g * 16 + q; wl[q] = __builtin_nontemporal_load(la0 + (size_t)t * (D / 2)); wb[q] = __builtin_nontemporal_load(bb0 + (size_t)t * (D / 2)); }
; #pragma unroll
;             for (int q = 0; q < 16; ++q) { const int t = g * 16 + q; hf0 = __expf(bf_lo(wl[q])) * hf0 + bf_lo(wb[q]); hf1 = __expf(bf_hi(wl[q])) * hf1 + bf_hi(wb[q]); fv0[t] = hf0; fv1[t] = hf1; } }
	v_permlane16_swap_b32_e32 v222, v223
	v_permlane16_swap_b32_e32 v224, v225
	v_permlane16_swap_b32_e32 v226, v227
	v_permlane16_swap_b32_e32 v228, v229
	v_permlane32_swap_b32_e32 v222, v224
	v_permlane32_swap_b32_e32 v223, v225
	v_permlane32_swap_b32_e32 v226, v228
	v_permlane32_swap_b32_e32 v227, v229
	v_and_b32_e32 v6, 0xffff0000, v222
	v_lshlrev_b32_e32 v222, 16, v222
	v_and_b32_e32 v7, 0xffff0000, v223
	v_lshlrev_b32_e32 v223, 16, v223
	v_and_b32_e32 v14, 0xffff0000, v224
	v_lshlrev_b32_e32 v224, 16, v224
	v_and_b32_e32 v15, 0xffff0000, v225
	v_lshlrev_b32_e32 v225, 16, v225
	v_mul_f32_e32 v222, 0x3fb8aa3b, v222
	v_mul_f32_e32 v6, 0x3fb8aa3b, v6
	v_mul_f32_e32 v223, 0x3fb8aa3b, v223
	v_mul_f32_e32 v7, 0x3fb8aa3b, v7
	v_mul_f32_e32 v224, 0x3fb8aa3b, v224
	v_mul_f32_e32 v14, 0x3fb8aa3b, v14
	v_mul_f32_e32 v225, 0x3fb8aa3b, v225
	v_mul_f32_e32 v15, 0x3fb8aa3b, v15
	v_exp_f32_e32 v222, v222
	v_exp_f32_e32 v6, v6
	v_exp_f32_e32 v223, v223
	v_exp_f32_e32 v7, v7
	v_exp_f32_e32 v224, v224
	v_exp_f32_e32 v14, v14
	v_exp_f32_e32 v225, v225
	v_exp_f32_e32 v15, v15
	v_lshlrev_b32_e32 v92, 16, v226
	v_and_b32_e32 v93, 0xffff0000, v226
	v_fmac_f32_e32 v92, v90, v222
	v_fmac_f32_e32 v93, v91, v6
	v_lshlrev_b32_e32 v94, 16, v227
	v_and_b32_e32 v95, 0xffff0000, v227
	v_fmac_f32_e32 v94, v92, v223
	v_fmac_f32_e32 v95, v93, v7
	v_lshlrev_b32_e32 v96, 16, v228
	v_and_b32_e32 v97, 0xffff0000, v228
	v_fmac_f32_e32 v96, v94, v224
	v_fmac_f32_e32 v97, v95, v14
	v_lshlrev_b32_e32 v98, 16, v229
	v_and_b32_e32 v99, 0xffff0000, v229
	v_fmac_f32_e32 v98, v96, v225
	v_fmac_f32_e32 v99, v97, v15
	global_load_dwordx4 v[222:225], v230, s[70:71] nt
	global_load_dwordx4 v[226:229], v230, s[72:73] nt
	v_add_u32_e32 v230, 0x2000, v230
	s_waitcnt vmcnt(6)
	v_permlane16_swap_b32_e32 v198, v199
	v_permlane16_swap_b32_e32 v200, v201
	v_permlane16_swap_b32_e32 v202, v203
	v_permlane16_swap_b32_e32 v204, v205
	v_permlane32_swap_b32_e32 v198, v200
	v_permlane32_swap_b32_e32 v199, v201
	v_permlane32_swap_b32_e32 v202, v204
	v_permlane32_swap_b32_e32 v203, v205
	v_and_b32_e32 v6, 0xffff0000, v198
	v_lshlrev_b32_e32 v198, 16, v198
	v_and_b32_e32 v7, 0xffff0000, v199
	v_lshlrev_b32_e32 v199, 16, v199
	v_and_b32_e32 v14, 0xffff0000, v200
	v_lshlrev_b32_e32 v200, 16, v200
	v_and_b32_e32 v15, 0xffff0000, v201
	v_lshlrev_b32_e32 v201, 16, v201
	v_mul_f32_e32 v198, 0x3fb8aa3b, v198
	v_mul_f32_e32 v6, 0x3fb8aa3b, v6
	v_mul_f32_e32 v199, 0x3fb8aa3b, v199
	v_mul_f32_e32 v7, 0x3fb8aa3b, v7
	v_mul_f32_e32 v200, 0x3fb8aa3b, v200
	v_mul_f32_e32 v14, 0x3fb8aa3b, v14
	v_mul_f32_e32 v201, 0x3fb8aa3b, v201
	v_mul_f32_e32 v15, 0x3fb8aa3b, v15
	v_exp_f32_e32 v198, v198
	v_exp_f32_e32 v6, v6
	v_exp_f32_e32 v199, v199
	v_exp_f32_e32 v7, v7
	v_exp_f32_e32 v200, v200
	v_exp_f32_e32 v14, v14
	v_exp_f32_e32 v201, v201
	v_exp_f32_e32 v15, v15
	v_lshlrev_b32_e32 v100, 16, v202
	v_and_b32_e32 v101, 0xffff0000, v202
	v_fmac_f32_e32 v100, v98, v198
	v_fmac_f32_e32 v101, v99, v6
	v_lshlrev_b32_e32 v102, 16, v203
	v_and_b32_e32 v103, 0xffff0000, v203
	v_fmac_f32_e32 v102, v100, v199
	v_fmac_f32_e32 v103, v101, v7
	v_lshlrev_b32_e32 v104, 16, v204
	v_and_b32_e32 v105, 0xffff0000, v204
	v_fmac_f32_e32 v104, v102, v200
	v_fmac_f32_e32 v105, v103, v14
	v_lshlrev_b32_e32 v106, 16, v205
	v_and_b32_e32 v107, 0xffff0000, v205
	v_fmac_f32_e32 v106, v104, v201
	v_fmac_f32_e32 v107, v105, v15
	global_load_dwordx4 v[198:201], v230, s[70:71] nt
	global_load_dwordx4 v[202:205], v230, s[72:73] nt
	v_add_u32_e32 v230, 0x2000, v230
	s_waitcnt vmcnt(6)
	v_permlane16_swap_b32_e32 v206, v207
	v_permlane16_swap_b32_e32 v208, v209
	v_permlane16_swap_b32_e32 v210, v211
	v_permlane16_swap_b32_e32 v212, v213
	v_permlane32_swap_b32_e32 v206, v208
	v_permlane32_swap_b32_e32 v207, v209
	v_permlane32_swap_b32_e32 v210, v212
	v_permlane32_swap_b32_e32 v211, v213
	v_and_b32_e32 v6, 0xffff0000, v206
	v_lshlrev_b32_e32 v206, 16, v206
	v_and_b32_e32 v7, 0xffff0000, v207
	v_lshlrev_b32_e32 v207, 16, v207
	v_and_b32_e32 v14, 0xffff0000, v208
	v_lshlrev_b32_e32 v208, 16, v208
	v_and_b32_e32 v15, 0xffff0000, v209
	v_lshlrev_b32_e32 v209, 16, v209
	v_mul_f32_e32 v206, 0x3fb8aa3b, v206
	v_mul_f32_e32 v6, 0x3fb8aa3b, v6
	v_mul_f32_e32 v207, 0x3fb8aa3b, v207
	v_mul_f32_e32 v7, 0x3fb8aa3b, v7
	v_mul_f32_e32 v208, 0x3fb8aa3b, v208
	v_mul_f32_e32 v14, 0x3fb8aa3b, v14
	v_mul_f32_e32 v209, 0x3fb8aa3b, v209
	v_mul_f32_e32 v15, 0x3fb8aa3b, v15
	v_exp_f32_e32 v206, v206
	v_exp_f32_e32 v6, v6
	v_exp_f32_e32 v207, v207
	v_exp_f32_e32 v7, v7
	v_exp_f32_e32 v208, v208
	v_exp_f32_e32 v14, v14
	v_exp_f32_e32 v209, v209
	v_exp_f32_e32 v15, v15
	v_lshlrev_b32_e32 v108, 16, v210
	v_and_b32_e32 v109, 0xffff0000, v210
	v_fmac_f32_e32 v108, v106, v206
	v_fmac_f32_e32 v109, v107, v6
	v_lshlrev_b32_e32 v110, 16, v211
	v_and_b32_e32 v111, 0xffff0000, v211
	v_fmac_f32_e32 v110, v108, v207
	v_fmac_f32_e32 v111, v109, v7
	v_lshlrev_b32_e32 v112, 16, v212
	v_and_b32_e32 v113, 0xffff0000, v212
	v_fmac_f32_e32 v112, v110, v208
	v_fmac_f32_e32 v113, v111, v14
	v_lshlrev_b32_e32 v114, 16, v213
	v_and_b32_e32 v115, 0xffff0000, v213
	v_fmac_f32_e32 v114, v112, v209
	v_fmac_f32_e32 v115, v113, v15
	global_load_dwordx4 v[206:209], v230, s[70:71] nt
	global_load_dwordx4 v[210:213], v230, s[72:73] nt
	v_add_u32_e32 v230, 0x2000, v230
	s_waitcnt vmcnt(6)
; __device__ __forceinline__ float bf_lo(unsigned w) { return __uint_as_float(w << 16); }
; __device__ __forceinline__ float bf_hi(unsigned w) { return __uint_as_float(w & 0xffff0000u); }
; __device__ __forceinline__ void scan_s3(CTXA) {
;     ...
;         for (int g = 0; g < 4; ++g) { unsigned wl[16], wb[16];
; #pragma unroll
;             for (int q = 0; q < 16; ++q) { const int t = g * 16 + q; wl[q] = __builtin_nontemporal_load(la0 + (size_t)t * (D / 2)); wb[q] = __builtin_nontemporal_load(bb0 + (size_t)t * (D / 2)); }
; #pragma unroll
;             for (int q = 0; q < 16; ++q) { const int t = g * 16 + q; hf0 = __expf(bf_lo(wl[q])) * hf0 + bf_lo(wb[q]); hf1 = __expf(bf_hi(wl[q])) * hf1 + bf_hi(wb[q]); fv0[t] = hf0; fv1[t] = hf1; } }
	v_permlane16_swap_b32_e32 v214, v215
	v_permlane16_swap_b32_e32 v216, v217
	v_permlane16_swap_b32_e32 v218, v219
	v_permlane16_swap_b32_e32 v220, v221
	v_permlane32_swap_b32_e32 v214, v216
	v_permlane32_swap_b32_e32 v215, v217
	v_permlane32_swap_b32_e32 v218, v220
	v_permlane32_swap_b32_e32 v219, v221
	v_and_b32_e32 v6, 0xffff0000, v214
	v_lshlrev_b32_e32 v214, 16, v214
	v_and_b32_e32 v7, 0xffff0000, v215
	v_lshlrev_b32_e32 v215, 16, v215
	v_and_b32_e32 v14, 0xffff0000, v216
	v_lshlrev_b32_e32 v216, 16, v216
	v_and_b32_e32 v15, 0xffff0000, v217
	v_lshlrev_b32_e32 v217, 16, v217
	v_mul_f32_e32 v214, 0x3fb8aa3b, v214
	v_mul_f32_e32 v6, 0x3fb8aa3b, v6
	v_mul_f32_e32 v215, 0x3fb8aa3b, v215
	v_mul_f32_e32 v7, 0x3fb8aa3b, v7
	v_mul_f32_e32 v216, 0x3fb8aa3b, v216
	v_mul_f32_e32 v14, 0x3fb8aa3b, v14
	v_mul_f32_e32 v217, 0x3fb8aa3b, v217
	v_mul_f32_e32 v15, 0x3fb8aa3b, v15
	v_exp_f32_e32 v214, v214
	v_exp_f32_e32 v6, v6
	v_exp_f32_e32 v215, v215
	v_exp_f32_e32 v7, v7
	v_exp_f32_e32 v216, v216
	v_exp_f32_e32 v14, v14
	v_exp_f32_e32 v217, v217
	v_exp_f32_e32 v15, v15
	v_lshlrev_b32_e32 v116, 16, v218
	v_and_b32_e32 v117, 0xffff0000, v218
	v_fmac_f32_e32 v116, v114, v214
	v_fmac_f32_e32 v117, v115, v6
	v_lshlrev_b32_e32 v118, 16, v219
	v_and_b32_e32 v119, 0xffff0000, v219
	v_fmac_f32_e32 v118, v116, v215
	v_fmac_f32_e32 v119, v117, v7
	v_lshlrev_b32_e32 v120, 16, v220
	v_and_b32_e32 v121, 0xffff0000, v220
	v_fmac_f32_e32 v120, v118, v216
	v_fmac_f32_e32 v121, v119, v14
	v_lshlrev_b32_e32 v122, 16, v221
	v_and_b32_e32 v123, 0xffff0000, v221
	v_fmac_f32_e32 v122, v120, v217
	v_fmac_f32_e32 v123, v121, v15
	global_load_dwordx4 v[214:217], v230, s[70:71] nt
	global_load_dwordx4 v[218:221], v230, s[72:73] nt
	v_add_u32_e32 v230, 0x2000, v230
	s_waitcnt vmcnt(6)
	v_permlane16_swap_b32_e32 v222, v223
	v_permlane16_swap_b32_e32 v224, v225
	v_permlane16_swap_b32_e32 v226, v227
	v_permlane16_swap_b32_e32 v228, v229
	v_permlane32_swap_b32_e32 v222, v224
	v_permlane32_swap_b32_e32 v223, v225
	v_permlane32_swap_b32_e32 v226, v228
	v_permlane32_swap_b32_e32 v227, v229
	v_and_b32_e32 v6, 0xffff0000, v222
	v_lshlrev_b32_e32 v222, 16, v222
	v_and_b32_e32 v7, 0xffff0000, v223
	v_lshlrev_b32_e32 v223, 16, v223
	v_and_b32_e32 v14, 0xffff0000, v224
	v_lshlrev_b32_e32 v224, 16, v224
	v_and_b32_e32 v15, 0xffff0000, v225
	v_lshlrev_b32_e32 v225, 16, v225
	v_mul_f32_e32 v222, 0x3fb8aa3b, v222
	v_mul_f32_e32 v6, 0x3fb8aa3b, v6
	v_mul_f32_e32 v223, 0x3fb8aa3b, v223
	v_mul_f32_e32 v7, 0x3fb8aa3b, v7
	v_mul_f32_e32 v224, 0x3fb8aa3b, v224
	v_mul_f32_e32 v14, 0x3fb8aa3b, v14
	v_mul_f32_e32 v225, 0x3fb8aa3b, v225
	v_mul_f32_e32 v15, 0x3fb8aa3b, v15
	v_exp_f32_e32 v222, v222
	v_exp_f32_e32 v6, v6
	v_exp_f32_e32 v223, v223
	v_exp_f32_e32 v7, v7
	v_exp_f32_e32 v224, v224
	v_exp_f32_e32 v14, v14
	v_exp_f32_e32 v225, v225
	v_exp_f32_e32 v15, v15
	v_lshlrev_b32_e32 v124, 16, v226
	v_and_b32_e32 v125, 0xffff0000, v226
	v_fmac_f32_e32 v124, v122, v222
	v_fmac_f32_e32 v125, v123, v6
	v_lshlrev_b32_e32 v126, 16, v227
	v_and_b32_e32 v127, 0xffff0000, v227
	v_fmac_f32_e32 v126, v124, v223
	v_fmac_f32_e32 v127, v125, v7
	v_lshlrev_b32_e32 v128, 16, v228
	v_and_b32_e32 v129, 0xffff0000, v228
	v_fmac_f32_e32 v128, v126, v224
	v_fmac_f32_e32 v129, v127, v14
	v_lshlrev_b32_e32 v130, 16, v229
	v_and_b32_e32 v131, 0xffff0000, v229
	v_fmac_f32_e32 v130, v128, v225
	v_fmac_f32_e32 v131, v129, v15
	global_load_dwordx4 v[222:225], v230, s[70:71] nt
	global_load_dwordx4 v[226:229], v230, s[72:73] nt
	v_add_u32_e32 v230, 0x2000, v230
	s_waitcnt vmcnt(6)
	v_permlane16_swap_b32_e32 v198, v199
	v_permlane16_swap_b32_e32 v200, v201
	v_permlane16_swap_b32_e32 v202, v203
	v_permlane16_swap_b32_e32 v204, v205
	v_permlane32_swap_b32_e32 v198, v200
	v_permlane32_swap_b32_e32 v199, v201
	v_permlane32_swap_b32_e32 v202, v204
	v_permlane32_swap_b32_e32 v203, v205
	v_and_b32_e32 v6, 0xffff0000, v198
	v_lshlrev_b32_e32 v198, 16, v198
	v_and_b32_e32 v7, 0xffff0000, v199
	v_lshlrev_b32_e32 v199, 16, v199
	v_and_b32_e32 v14, 0xffff0000, v200
	v_lshlrev_b32_e32 v200, 16, v200
	v_and_b32_e32 v15, 0xffff0000, v201
	v_lshlrev_b32_e32 v201, 16, v201
	v_mul_f32_e32 v198, 0x3fb8aa3b, v198
	v_mul_f32_e32 v6, 0x3fb8aa3b, v6
	v_mul_f32_e32 v199, 0x3fb8aa3b, v199
	v_mul_f32_e32 v7, 0x3fb8aa3b, v7
	v_mul_f32_e32 v200, 0x3fb8aa3b, v200
	v_mul_f32_e32 v14, 0x3fb8aa3b, v14
	v_mul_f32_e32 v201, 0x3fb8aa3b, v201
	v_mul_f32_e32 v15, 0x3fb8aa3b, v15
	v_exp_f32_e32 v198, v198
	v_exp_f32_e32 v6, v6
	v_exp_f32_e32 v199, v199
	v_exp_f32_e32 v7, v7
	v_exp_f32_e32 v200, v200
	v_exp_f32_e32 v14, v14
	v_exp_f32_e32 v201, v201
	v_exp_f32_e32 v15, v15
	v_lshlrev_b32_e32 v132, 16, v202
	v_and_b32_e32 v133, 0xffff0000, v202
	v_fmac_f32_e32 v132, v130, v198
	v_fmac_f32_e32 v133, v131, v6
	v_lshlrev_b32_e32 v134, 16, v203
	v_and_b32_e32 v135, 0xffff0000, v203
	v_fmac_f32_e32 v134, v132, v199
	v_fmac_f32_e32 v135, v133, v7
	v_lshlrev_b32_e32 v136, 16, v204
	v_and_b32_e32 v137, 0xffff0000, v204
	v_fmac_f32_e32 v136, v134, v200
	v_fmac_f32_e32 v137, v135, v14
	v_lshlrev_b32_e32 v138, 16, v205
	v_and_b32_e32 v139, 0xffff0000, v205
	v_fmac_f32_e32 v138, v136, v201
	v_fmac_f32_e32 v139, v137, v15
	global_load_dwordx4 v[198:201], v230, s[70:71] nt
	global_load_dwordx4 v[202:205], v230, s[72:73] nt
	v_add_u32_e32 v230, 0x2000, v230
	s_waitcnt vmcnt(6)
; __device__ __forceinline__ float bf_lo(unsigned w) { return __uint_as_float(w << 16); }
; __device__ __forceinline__ float bf_hi(unsigned w) { return __uint_as_float(w & 0xffff0000u); }
; __device__ __forceinline__ void scan_s3(CTXA) {
;     ...
;         for (int g = 0; g < 4; ++g) { unsigned wl[16], wb[16];
; #pragma unroll
;             for (int q = 0; q < 16; ++q) { const int t = g * 16 + q; wl[q] = __builtin_nontemporal_load(la0 + (size_t)t * (D / 2)); wb[q] = __builtin_nontemporal_load(bb0 + (size_t)t * (D / 2)); }
; #pragma unroll
;             for (int q = 0; q < 16; ++q) { const int t = g * 16 + q; hf0 = __expf(bf_lo(wl[q])) * hf0 + bf_lo(wb[q]); hf1 = __expf(bf_hi(wl[q])) * hf1 + bf_hi(wb[q]); fv0[t] = hf0; fv1[t] = hf1; } }
	v_permlane16_swap_b32_e32 v206, v207
	v_permlane16_swap_b32_e32 v208, v209
	v_permlane16_swap_b32_e32 v210, v211
	v_permlane16_swap_b32_e32 v212, v213
	v_permlane32_swap_b32_e32 v206, v208
	v_permlane32_swap_b32_e32 v207, v209
	v_permlane32_swap_b32_e32 v210, v212
	v_permlane32_swap_b32_e32 v211, v213
	v_and_b32_e32 v6, 0xffff0000, v206
	v_lshlrev_b32_e32 v206, 16, v206
	v_and_b32_e32 v7, 0xffff0000, v207
	v_lshlrev_b32_e32 v207, 16, v207
	v_and_b32_e32 v14, 0xffff0000, v208
	v_lshlrev_b32_e32 v208, 16, v208
	v_and_b32_e32 v15, 0xffff0000, v209
	v_lshlrev_b32_e32 v209, 16, v209
	v_mul_f32_e32 v206, 0x3fb8aa3b, v206
	v_mul_f32_e32 v6, 0x3fb8aa3b, v6
	v_mul_f32_e32 v207, 0x3fb8aa3b, v207
	v_mul_f32_e32 v7, 0x3fb8aa3b, v7
	v_mul_f32_e32 v208, 0x3fb8aa3b, v208
	v_mul_f32_e32 v14, 0x3fb8aa3b, v14
	v_mul_f32_e32 v209, 0x3fb8aa3b, v209
	v_mul_f32_e32 v15, 0x3fb8aa3b, v15
	v_exp_f32_e32 v206, v206
	v_exp_f32_e32 v6, v6
	v_exp_f32_e32 v207, v207
	v_exp_f32_e32 v7, v7
	v_exp_f32_e32 v208, v208
	v_exp_f32_e32 v14, v14
	v_exp_f32_e32 v209, v209
	v_exp_f32_e32 v15, v15
	v_lshlrev_b32_e32 v140, 16, v210
	v_and_b32_e32 v141, 0xffff0000, v210
	v_fmac_f32_e32 v140, v138, v206
	v_fmac_f32_e32 v141, v139, v6
	v_lshlrev_b32_e32 v142, 16, v211
	v_and_b32_e32 v143, 0xffff0000, v211
	v_fmac_f32_e32 v142, v140, v207
	v_fmac_f32_e32 v143, v141, v7
	v_lshlrev_b32_e32 v144, 16, v212
	v_and_b32_e32 v145, 0xffff0000, v212
	v_fmac_f32_e32 v144, v142, v208
	v_fmac_f32_e32 v145, v143, v14
	v_lshlrev_b32_e32 v146, 16, v213
	v_and_b32_e32 v147, 0xffff0000, v213
	v_fmac_f32_e32 v146, v144, v209
	v_fmac_f32_e32 v147, v145, v15
	global_load_dwordx4 v[206:209], v230, s[70:71] nt
	global_load_dwordx4 v[210:213], v230, s[72:73] nt
	v_add_u32_e32 v230, 0x2000, v230
	s_waitcnt vmcnt(6)
	v_permlane16_swap_b32_e32 v214, v215
	v_permlane16_swap_b32_e32 v216, v217
	v_permlane16_swap_b32_e32 v218, v219
	v_permlane16_swap_b32_e32 v220, v221
	v_permlane32_swap_b32_e32 v214, v216
	v_permlane32_swap_b32_e32 v215, v217
	v_permlane32_swap_b32_e32 v218, v220
	v_permlane32_swap_b32_e32 v219, v221
	v_and_b32_e32 v6, 0xffff0000, v214
	v_lshlrev_b32_e32 v214, 16, v214
	v_and_b32_e32 v7, 0xffff0000, v215
	v_lshlrev_b32_e32 v215, 16, v215
	v_and_b32_e32 v14, 0xffff0000, v216
	v_lshlrev_b32_e32 v216, 16, v216
	v_and_b32_e32 v15, 0xffff0000, v217
	v_lshlrev_b32_e32 v217, 16, v217
	v_mul_f32_e32 v214, 0x3fb8aa3b, v214
	v_mul_f32_e32 v6, 0x3fb8aa3b, v6
	v_mul_f32_e32 v215, 0x3fb8aa3b, v215
	v_mul_f32_e32 v7, 0x3fb8aa3b, v7
	v_mul_f32_e32 v216, 0x3fb8aa3b, v216
	v_mul_f32_e32 v14, 0x3fb8aa3b, v14
	v_mul_f32_e32 v217, 0x3fb8aa3b, v217
	v_mul_f32_e32 v15, 0x3fb8aa3b, v15
	v_exp_f32_e32 v214, v214
	v_exp_f32_e32 v6, v6
	v_exp_f32_e32 v215, v215
	v_exp_f32_e32 v7, v7
	v_exp_f32_e32 v216, v216
	v_exp_f32_e32 v14, v14
	v_exp_f32_e32 v217, v217
	v_exp_f32_e32 v15, v15
	v_lshlrev_b32_e32 v148, 16, v218
	v_and_b32_e32 v149, 0xffff0000, v218
	v_fmac_f32_e32 v148, v146, v214
	v_fmac_f32_e32 v149, v147, v6
	v_lshlrev_b32_e32 v150, 16, v219
	v_and_b32_e32 v151, 0xffff0000, v219
	v_fmac_f32_e32 v150, v148, v215
	v_fmac_f32_e32 v151, v149, v7
	v_lshlrev_b32_e32 v152, 16, v220
	v_and_b32_e32 v153, 0xffff0000, v220
	v_fmac_f32_e32 v152, v150, v216
	v_fmac_f32_e32 v153, v151, v14
	v_lshlrev_b32_e32 v154, 16, v221
	v_and_b32_e32 v155, 0xffff0000, v221
	v_fmac_f32_e32 v154, v152, v217
	v_fmac_f32_e32 v155, v153, v15
	global_load_dwordx4 v[214:217], v230, s[70:71] nt
	global_load_dwordx4 v[218:221], v230, s[72:73] nt
	v_add_u32_e32 v230, 0x2000, v230
	s_waitcnt vmcnt(6)
	v_permlane16_swap_b32_e32 v222, v223
	v_permlane16_swap_b32_e32 v224, v225
	v_permlane16_swap_b32_e32 v226, v227
	v_permlane16_swap_b32_e32 v228, v229
	v_permlane32_swap_b32_e32 v222, v224
	v_permlane32_swap_b32_e32 v223, v225
	v_permlane32_swap_b32_e32 v226, v228
	v_permlane32_swap_b32_e32 v227, v229
	v_and_b32_e32 v6, 0xffff0000, v222
	v_lshlrev_b32_e32 v222, 16, v222
	v_and_b32_e32 v7, 0xffff0000, v223
	v_lshlrev_b32_e32 v223, 16, v223
	v_and_b32_e32 v14, 0xffff0000, v224
	v_lshlrev_b32_e32 v224, 16, v224
	v_and_b32_e32 v15, 0xffff0000, v225
	v_lshlrev_b32_e32 v225, 16, v225
	v_mul_f32_e32 v222, 0x3fb8aa3b, v222
	v_mul_f32_e32 v6, 0x3fb8aa3b, v6
	v_mul_f32_e32 v223, 0x3fb8aa3b, v223
	v_mul_f32_e32 v7, 0x3fb8aa3b, v7
	v_mul_f32_e32 v224, 0x3fb8aa3b, v224
	v_mul_f32_e32 v14, 0x3fb8aa3b, v14
	v_mul_f32_e32 v225, 0x3fb8aa3b, v225
	v_mul_f32_e32 v15, 0x3fb8aa3b, v15
	v_exp_f32_e32 v222, v222
	v_exp_f32_e32 v6, v6
	v_exp_f32_e32 v223, v223
	v_exp_f32_e32 v7, v7
	v_exp_f32_e32 v224, v224
	v_exp_f32_e32 v14, v14
	v_exp_f32_e32 v225, v225
	v_exp_f32_e32 v15, v15
	v_lshlrev_b32_e32 v156, 16, v226
	v_and_b32_e32 v157, 0xffff0000, v226
	v_fmac_f32_e32 v156, v154, v222
	v_fmac_f32_e32 v157, v155, v6
	v_lshlrev_b32_e32 v158, 16, v227
	v_and_b32_e32 v159, 0xffff0000, v227
	v_fmac_f32_e32 v158, v156, v223
	v_fmac_f32_e32 v159, v157, v7
	v_lshlrev_b32_e32 v160, 16, v228
	v_and_b32_e32 v161, 0xffff0000, v228
	v_fmac_f32_e32 v160, v158, v224
	v_fmac_f32_e32 v161, v159, v14
	v_lshlrev_b32_e32 v162, 16, v229
	v_and_b32_e32 v163, 0xffff0000, v229
	v_fmac_f32_e32 v162, v160, v225
	v_fmac_f32_e32 v163, v161, v15
	global_load_dwordx4 v[222:225], v230, s[70:71] nt
	global_load_dwordx4 v[226:229], v230, s[72:73] nt
	s_waitcnt vmcnt(6)
; __device__ __forceinline__ float bf_lo(unsigned w) { return __uint_as_float(w << 16); }
; __device__ __forceinline__ float bf_hi(unsigned w) { return __uint_as_float(w & 0xffff0000u); }
; __device__ __forceinline__ void scan_s3(CTXA) {
;     ...
;         for (int g = 0; g < 4; ++g) { unsigned wl[16], wb[16];
; #pragma unroll
;             for (int q = 0; q < 16; ++q) { const int t = g * 16 + q; wl[q] = __builtin_nontemporal_load(la0 + (size_t)t * (D / 2)); wb[q] = __builtin_nontemporal_load(bb0 + (size_t)t * (D / 2)); }
; #pragma unroll
;             for (int q = 0; q < 16; ++q) { const int t = g * 16 + q; hf0 = __expf(bf_lo(wl[q])) * hf0 + bf_lo(wb[q]); hf1 = __expf(bf_hi(wl[q])) * hf1 + bf_hi(wb[q]); fv0[t] = hf0; fv1[t] = hf1; } }
	v_permlane16_swap_b32_e32 v198, v199
	v_permlane16_swap_b32_e32 v200, v201
	v_permlane16_swap_b32_e32 v202, v203
	v_permlane16_swap_b32_e32 v204, v205
	v_permlane32_swap_b32_e32 v198, v200
	v_permlane32_swap_b32_e32 v199, v201
	v_permlane32_swap_b32_e32 v202, v204
	v_permlane32_swap_b32_e32 v203, v205
	v_and_b32_e32 v6, 0xffff0000, v198
	v_lshlrev_b32_e32 v198, 16, v198
	v_and_b32_e32 v7, 0xffff0000, v199
	v_lshlrev_b32_e32 v199, 16, v199
	v_and_b32_e32 v14, 0xffff0000, v200
	v_lshlrev_b32_e32 v200, 16, v200
	v_and_b32_e32 v15, 0xffff0000, v201
	v_lshlrev_b32_e32 v201, 16, v201
	v_mul_f32_e32 v198, 0x3fb8aa3b, v198
	v_mul_f32_e32 v6, 0x3fb8aa3b, v6
	v_mul_f32_e32 v199, 0x3fb8aa3b, v199
	v_mul_f32_e32 v7, 0x3fb8aa3b, v7
	v_mul_f32_e32 v200, 0x3fb8aa3b, v200
	v_mul_f32_e32 v14, 0x3fb8aa3b, v14
	v_mul_f32_e32 v201, 0x3fb8aa3b, v201
	v_mul_f32_e32 v15, 0x3fb8aa3b, v15
	v_exp_f32_e32 v198, v198
	v_exp_f32_e32 v6, v6
	v_exp_f32_e32 v199, v199
	v_exp_f32_e32 v7, v7
	v_exp_f32_e32 v200, v200
	v_exp_f32_e32 v14, v14
	v_exp_f32_e32 v201, v201
	v_exp_f32_e32 v15, v15
	v_lshlrev_b32_e32 v164, 16, v202
	v_and_b32_e32 v165, 0xffff0000, v202
	v_fmac_f32_e32 v164, v162, v198
	v_fmac_f32_e32 v165, v163, v6
	v_lshlrev_b32_e32 v166, 16, v203
	v_and_b32_e32 v167, 0xffff0000, v203
	v_fmac_f32_e32 v166, v164, v199
	v_fmac_f32_e32 v167, v165, v7
	v_lshlrev_b32_e32 v168, 16, v204
	v_and_b32_e32 v169, 0xffff0000, v204
	v_fmac_f32_e32 v168, v166, v200
	v_fmac_f32_e32 v169, v167, v14
	v_lshlrev_b32_e32 v170, 16, v205
	v_and_b32_e32 v171, 0xffff0000, v205
	v_fmac_f32_e32 v170, v168, v201
	v_fmac_f32_e32 v171, v169, v15
	s_waitcnt vmcnt(4)
	v_permlane16_swap_b32_e32 v206, v207
	v_permlane16_swap_b32_e32 v208, v209
	v_permlane16_swap_b32_e32 v210, v211
	v_permlane16_swap_b32_e32 v212, v213
	v_permlane32_swap_b32_e32 v206, v208
	v_permlane32_swap_b32_e32 v207, v209
	v_permlane32_swap_b32_e32 v210, v212
	v_permlane32_swap_b32_e32 v211, v213
	v_and_b32_e32 v6, 0xffff0000, v206
	v_lshlrev_b32_e32 v206, 16, v206
	v_and_b32_e32 v7, 0xffff0000, v207
	v_lshlrev_b32_e32 v207, 16, v207
	v_and_b32_e32 v14, 0xffff0000, v208
	v_lshlrev_b32_e32 v208, 16, v208
	v_and_b32_e32 v15, 0xffff0000, v209
	v_lshlrev_b32_e32 v209, 16, v209
	v_mul_f32_e32 v206, 0x3fb8aa3b, v206
	v_mul_f32_e32 v6, 0x3fb8aa3b, v6
	v_mul_f32_e32 v207, 0x3fb8aa3b, v207
	v_mul_f32_e32 v7, 0x3fb8aa3b, v7
	v_mul_f32_e32 v208, 0x3fb8aa3b, v208
	v_mul_f32_e32 v14, 0x3fb8aa3b, v14
	v_mul_f32_e32 v209, 0x3fb8aa3b, v209
	v_mul_f32_e32 v15, 0x3fb8aa3b, v15
	v_exp_f32_e32 v206, v206
	v_exp_f32_e32 v6, v6
	v_exp_f32_e32 v207, v207
	v_exp_f32_e32 v7, v7
	v_exp_f32_e32 v208, v208
	v_exp_f32_e32 v14, v14
	v_exp_f32_e32 v209, v209
	v_exp_f32_e32 v15, v15
	v_lshlrev_b32_e32 v172, 16, v210
	v_and_b32_e32 v173, 0xffff0000, v210
	v_fmac_f32_e32 v172, v170, v206
	v_fmac_f32_e32 v173, v171, v6
	v_lshlrev_b32_e32 v174, 16, v211
	v_and_b32_e32 v175, 0xffff0000, v211
	v_fmac_f32_e32 v174, v172, v207
	v_fmac_f32_e32 v175, v173, v7
	v_lshlrev_b32_e32 v176, 16, v212
	v_and_b32_e32 v177, 0xffff0000, v212
	v_fmac_f32_e32 v176, v174, v208
	v_fmac_f32_e32 v177, v175, v14
	v_lshlrev_b32_e32 v178, 16, v213
	v_and_b32_e32 v179, 0xffff0000, v213
	v_fmac_f32_e32 v178, v176, v209
	v_fmac_f32_e32 v179, v177, v15
	s_waitcnt vmcnt(2)
	v_permlane16_swap_b32_e32 v214, v215
	v_permlane16_swap_b32_e32 v216, v217
	v_permlane16_swap_b32_e32 v218, v219
	v_permlane16_swap_b32_e32 v220, v221
	v_permlane32_swap_b32_e32 v214, v216
	v_permlane32_swap_b32_e32 v215, v217
	v_permlane32_swap_b32_e32 v218, v220
	v_permlane32_swap_b32_e32 v219, v221
	v_and_b32_e32 v6, 0xffff0000, v214
	v_lshlrev_b32_e32 v214, 16, v214
	v_and_b32_e32 v7, 0xffff0000, v215
	v_lshlrev_b32_e32 v215, 16, v215
	v_and_b32_e32 v14, 0xffff0000, v216
	v_lshlrev_b32_e32 v216, 16, v216
	v_and_b32_e32 v15, 0xffff0000, v217
	v_lshlrev_b32_e32 v217, 16, v217
	v_mul_f32_e32 v214, 0x3fb8aa3b, v214
	v_mul_f32_e32 v6, 0x3fb8aa3b, v6
	v_mul_f32_e32 v215, 0x3fb8aa3b, v215
	v_mul_f32_e32 v7, 0x3fb8aa3b, v7
	v_mul_f32_e32 v216, 0x3fb8aa3b, v216
	v_mul_f32_e32 v14, 0x3fb8aa3b, v14
	v_mul_f32_e32 v217, 0x3fb8aa3b, v217
	v_mul_f32_e32 v15, 0x3fb8aa3b, v15
	v_exp_f32_e32 v214, v214
	v_exp_f32_e32 v6, v6
	v_exp_f32_e32 v215, v215
	v_exp_f32_e32 v7, v7
	v_exp_f32_e32 v216, v216
	v_exp_f32_e32 v14, v14
	v_exp_f32_e32 v217, v217
	v_exp_f32_e32 v15, v15
	v_lshlrev_b32_e32 v180, 16, v218
	v_and_b32_e32 v181, 0xffff0000, v218
	v_fmac_f32_e32 v180, v178, v214
	v_fmac_f32_e32 v181, v179, v6
	v_lshlrev_b32_e32 v182, 16, v219
	v_and_b32_e32 v183, 0xffff0000, v219
	v_fmac_f32_e32 v182, v180, v215
	v_fmac_f32_e32 v183, v181, v7
	v_lshlrev_b32_e32 v184, 16, v220
	v_and_b32_e32 v185, 0xffff0000, v220
	v_fmac_f32_e32 v184, v182, v216
	v_fmac_f32_e32 v185, v183, v14
	v_lshlrev_b32_e32 v186, 16, v221
	v_and_b32_e32 v187, 0xffff0000, v221
	v_fmac_f32_e32 v186, v184, v217
	v_fmac_f32_e32 v187, v185, v15
	s_waitcnt vmcnt(0)
; __device__ __forceinline__ unsigned cvt_pk_bf16(float lo, float hi) { unsigned r; asm("v_cvt_pk_bf16_f32 %0, %1, %2" : "=v"(r) : "v"(lo), "v"(hi)); return r; }
; __device__ __forceinline__ float bf_lo(unsigned w) { return __uint_as_float(w << 16); }
; __device__ __forceinline__ float bf_hi(unsigned w) { return __uint_as_float(w & 0xffff0000u); }
; __device__ __forceinline__ void scan_s3(CTXA) {
;     ...
;         for (int g = 0; g < 4; ++g) { unsigned wl[16], wb[16], wg[16];
; #pragma unroll
;             for (int q = 0; q < 16; ++q) { const int t = 63 - (g * 16 + q); wl[q] = __builtin_nontemporal_load(la1 + (size_t)t * (D / 2)); wb[q] = __builtin_nontemporal_load(bb1 + (size_t)t * (D / 2)); wg[q] = __builtin_nontemporal_load(gg + (size_t)t * (D / 2)); }
; #pragma unroll
;             for (int q = 0; q < 16; ++q) { const int t = 63 - (g * 16 + q); hb0 = __expf(bf_lo(wl[q])) * hb0 + bf_lo(wb[q]); hb1 = __expf(bf_hi(wl[q])) * hb1 + bf_hi(wb[q]);
;                 yy[(size_t)t * (D / 2)] = cvt_pk_bf16((fv0[t] + hb0) * bf_lo(wg[q]), (fv1[t] + hb1) * bf_hi(wg[q])); } }
	v_permlane16_swap_b32_e32 v222, v223
	v_permlane16_swap_b32_e32 v224, v225
	v_permlane16_swap_b32_e32 v226, v227
	v_permlane16_swap_b32_e32 v228, v229
	v_permlane32_swap_b32_e32 v222, v224
	v_permlane32_swap_b32_e32 v223, v225
	v_permlane32_swap_b32_e32 v226, v228
	v_permlane32_swap_b32_e32 v227, v229
	v_and_b32_e32 v6, 0xffff0000, v222
	v_lshlrev_b32_e32 v222, 16, v222
	v_and_b32_e32 v7, 0xffff0000, v223
	v_lshlrev_b32_e32 v223, 16, v223
	v_and_b32_e32 v14, 0xffff0000, v224
	v_lshlrev_b32_e32 v224, 16, v224
	v_and_b32_e32 v15, 0xffff0000, v225
	v_lshlrev_b32_e32 v225, 16, v225
	v_mul_f32_e32 v222, 0x3fb8aa3b, v222
	v_mul_f32_e32 v6, 0x3fb8aa3b, v6
	v_mul_f32_e32 v223, 0x3fb8aa3b, v223
	v_mul_f32_e32 v7, 0x3fb8aa3b, v7
	v_mul_f32_e32 v224, 0x3fb8aa3b, v224
	v_mul_f32_e32 v14, 0x3fb8aa3b, v14
	v_mul_f32_e32 v225, 0x3fb8aa3b, v225
	v_mul_f32_e32 v15, 0x3fb8aa3b, v15
	v_exp_f32_e32 v222, v222
	v_exp_f32_e32 v6, v6
	v_exp_f32_e32 v223, v223
	v_exp_f32_e32 v7, v7
	v_exp_f32_e32 v224, v224
	v_exp_f32_e32 v14, v14
	v_exp_f32_e32 v225, v225
	v_exp_f32_e32 v15, v15
	v_lshlrev_b32_e32 v188, 16, v226
	v_and_b32_e32 v189, 0xffff0000, v226
	v_fmac_f32_e32 v188, v186, v222
	v_fmac_f32_e32 v189, v187, v6
	v_lshlrev_b32_e32 v190, 16, v227
	v_and_b32_e32 v191, 0xffff0000, v227
	v_fmac_f32_e32 v190, v188, v223
	v_fmac_f32_e32 v191, v189, v7
	v_lshlrev_b32_e32 v192, 16, v228
	v_and_b32_e32 v193, 0xffff0000, v228
	v_fmac_f32_e32 v192, v190, v224
	v_fmac_f32_e32 v193, v191, v14
	v_lshlrev_b32_e32 v194, 16, v229
	v_and_b32_e32 v195, 0xffff0000, v229
	v_fmac_f32_e32 v194, v192, v225
	v_fmac_f32_e32 v195, v193, v15
	s_waitcnt vmcnt(33)
	v_permlane16_swap_b32_e32 v18, v19
	v_permlane16_swap_b32_e32 v20, v21
	v_permlane16_swap_b32_e32 v22, v23
	v_permlane16_swap_b32_e32 v24, v25
	v_permlane16_swap_b32_e32 v26, v27
	v_permlane16_swap_b32_e32 v28, v29
	v_permlane32_swap_b32_e32 v18, v20
	v_permlane32_swap_b32_e32 v19, v21
	v_permlane32_swap_b32_e32 v22, v24
	v_permlane32_swap_b32_e32 v23, v25
	v_permlane32_swap_b32_e32 v26, v28
	v_permlane32_swap_b32_e32 v27, v29
	v_and_b32_e32 v6, 0xffff0000, v18
	v_lshlrev_b32_e32 v18, 16, v18
	v_and_b32_e32 v7, 0xffff0000, v19
	v_lshlrev_b32_e32 v19, 16, v19
	v_and_b32_e32 v14, 0xffff0000, v20
	v_lshlrev_b32_e32 v20, 16, v20
	v_and_b32_e32 v15, 0xffff0000, v21
	v_lshlrev_b32_e32 v21, 16, v21
	v_mul_f32_e32 v18, 0x3fb8aa3b, v18
	v_mul_f32_e32 v6, 0x3fb8aa3b, v6
	v_mul_f32_e32 v19, 0x3fb8aa3b, v19
	v_mul_f32_e32 v7, 0x3fb8aa3b, v7
	v_mul_f32_e32 v20, 0x3fb8aa3b, v20
	v_mul_f32_e32 v14, 0x3fb8aa3b, v14
	v_mul_f32_e32 v21, 0x3fb8aa3b, v21
	v_mul_f32_e32 v15, 0x3fb8aa3b, v15
	v_exp_f32_e32 v18, v18
	v_exp_f32_e32 v6, v6
	v_exp_f32_e32 v19, v19
	v_exp_f32_e32 v7, v7
	v_exp_f32_e32 v20, v20
	v_exp_f32_e32 v14, v14
	v_exp_f32_e32 v21, v21
	v_exp_f32_e32 v15, v15
	v_lshlrev_b32_e32 v12, 16, v25
	v_and_b32_e32 v13, 0xffff0000, v25
	v_fmac_f32_e32 v12, v10, v21
	v_fmac_f32_e32 v13, v11, v15
	v_lshlrev_b32_e32 v17, 16, v29
	v_and_b32_e32 v29, 0xffff0000, v29
	v_add_f32_e32 v194, v194, v12
	v_add_f32_e32 v195, v195, v13
	v_mul_f32_e32 v194, v194, v17
	v_mul_f32_e32 v195, v195, v29
	v_cvt_pk_bf16_f32 v29, v194, v195
	v_lshlrev_b32_e32 v10, 16, v24
	v_and_b32_e32 v11, 0xffff0000, v24
	v_fmac_f32_e32 v10, v12, v20
	v_fmac_f32_e32 v11, v13, v14
	v_lshlrev_b32_e32 v17, 16, v28
	v_and_b32_e32 v28, 0xffff0000, v28
	v_add_f32_e32 v192, v192, v10
	v_add_f32_e32 v193, v193, v11
	v_mul_f32_e32 v192, v192, v17
	v_mul_f32_e32 v193, v193, v28
	v_cvt_pk_bf16_f32 v28, v192, v193
	v_lshlrev_b32_e32 v12, 16, v23
	v_and_b32_e32 v13, 0xffff0000, v23
	v_fmac_f32_e32 v12, v10, v19
	v_fmac_f32_e32 v13, v11, v7
	v_lshlrev_b32_e32 v17, 16, v27
	v_and_b32_e32 v27, 0xffff0000, v27
	v_add_f32_e32 v190, v190, v12
	v_add_f32_e32 v191, v191, v13
	v_mul_f32_e32 v190, v190, v17
	v_mul_f32_e32 v191, v191, v27
	v_cvt_pk_bf16_f32 v27, v190, v191
	v_lshlrev_b32_e32 v10, 16, v22
	v_and_b32_e32 v11, 0xffff0000, v22
	v_fmac_f32_e32 v10, v12, v18
	v_fmac_f32_e32 v11, v13, v6
	v_lshlrev_b32_e32 v17, 16, v26
	v_and_b32_e32 v26, 0xffff0000, v26
	v_add_f32_e32 v188, v188, v10
	v_add_f32_e32 v189, v189, v11
	v_mul_f32_e32 v188, v188, v17
	v_mul_f32_e32 v189, v189, v26
	v_cvt_pk_bf16_f32 v26, v188, v189
	s_nop 1
	v_permlane16_swap_b32_e32 v26, v27
	v_permlane16_swap_b32_e32 v28, v29
	s_nop 1
	v_permlane32_swap_b32_e32 v26, v28
	v_permlane32_swap_b32_e32 v27, v29
	global_store_dwordx4 v232, v[26:29], s[80:81]
	v_add_u32_e32 v232, 0xffffe000, v232
	global_load_dwordx4 v[18:21], v231, s[82:83] nt
	global_load_dwordx4 v[22:25], v231, s[84:85] nt
	global_load_dwordx4 v[26:29], v231, s[78:79] nt
	v_add_u32_e32 v231, 0xffffe000, v231
	s_waitcnt vmcnt(34)
; __device__ __forceinline__ unsigned cvt_pk_bf16(float lo, float hi) { unsigned r; asm("v_cvt_pk_bf16_f32 %0, %1, %2" : "=v"(r) : "v"(lo), "v"(hi)); return r; }
; __device__ __forceinline__ float bf_lo(unsigned w) { return __uint_as_float(w << 16); }
; __device__ __forceinline__ float bf_hi(unsigned w) { return __uint_as_float(w & 0xffff0000u); }
; __device__ __forceinline__ void scan_s3(CTXA) {
;     ...
;         for (int g = 0; g < 4; ++g) { unsigned wl[16], wb[16], wg[16];
; #pragma unroll
;             for (int q = 0; q < 16; ++q) { const int t = 63 - (g * 16 + q); wl[q] = __builtin_nontemporal_load(la1 + (size_t)t * (D / 2)); wb[q] = __builtin_nontemporal_load(bb1 + (size_t)t * (D / 2)); wg[q] = __builtin_nontemporal_load(gg + (size_t)t * (D / 2)); }
; #pragma unroll
;             for (int q = 0; q < 16; ++q) { const int t = 63 - (g * 16 + q); hb0 = __expf(bf_lo(wl[q])) * hb0 + bf_lo(wb[q]); hb1 = __expf(bf_hi(wl[q])) * hb1 + bf_hi(wb[q]);
;                 yy[(size_t)t * (D / 2)] = cvt_pk_bf16((fv0[t] + hb0) * bf_lo(wg[q]), (fv1[t] + hb1) * bf_hi(wg[q])); } }
	v_permlane16_swap_b32_e32 v30, v31
	v_permlane16_swap_b32_e32 v32, v33
	v_permlane16_swap_b32_e32 v34, v35
	v_permlane16_swap_b32_e32 v36, v37
	v_permlane16_swap_b32_e32 v38, v39
	v_permlane16_swap_b32_e32 v40, v41
	v_permlane32_swap_b32_e32 v30, v32
	v_permlane32_swap_b32_e32 v31, v33
	v_permlane32_swap_b32_e32 v34, v36
	v_permlane32_swap_b32_e32 v35, v37
	v_permlane32_swap_b32_e32 v38, v40
	v_permlane32_swap_b32_e32 v39, v41
	v_and_b32_e32 v6, 0xffff0000, v30
	v_lshlrev_b32_e32 v30, 16, v30
	v_and_b32_e32 v7, 0xffff0000, v31
	v_lshlrev_b32_e32 v31, 16, v31
	v_and_b32_e32 v14, 0xffff0000, v32
	v_lshlrev_b32_e32 v32, 16, v32
	v_and_b32_e32 v15, 0xffff0000, v33
	v_lshlrev_b32_e32 v33, 16, v33
	v_mul_f32_e32 v30, 0x3fb8aa3b, v30
	v_mul_f32_e32 v6, 0x3fb8aa3b, v6
	v_mul_f32_e32 v31, 0x3fb8aa3b, v31
	v_mul_f32_e32 v7, 0x3fb8aa3b, v7
	v_mul_f32_e32 v32, 0x3fb8aa3b, v32
	v_mul_f32_e32 v14, 0x3fb8aa3b, v14
	v_mul_f32_e32 v33, 0x3fb8aa3b, v33
	v_mul_f32_e32 v15, 0x3fb8aa3b, v15
	v_exp_f32_e32 v30, v30
	v_exp_f32_e32 v6, v6
	v_exp_f32_e32 v31, v31
	v_exp_f32_e32 v7, v7
	v_exp_f32_e32 v32, v32
	v_exp_f32_e32 v14, v14
	v_exp_f32_e32 v33, v33
	v_exp_f32_e32 v15, v15
	v_lshlrev_b32_e32 v12, 16, v37
	v_and_b32_e32 v13, 0xffff0000, v37
	v_fmac_f32_e32 v12, v10, v33
	v_fmac_f32_e32 v13, v11, v15
	v_lshlrev_b32_e32 v17, 16, v41
	v_and_b32_e32 v41, 0xffff0000, v41
	v_add_f32_e32 v186, v186, v12
	v_add_f32_e32 v187, v187, v13
	v_mul_f32_e32 v186, v186, v17
	v_mul_f32_e32 v187, v187, v41
	v_cvt_pk_bf16_f32 v41, v186, v187
	v_lshlrev_b32_e32 v10, 16, v36
	v_and_b32_e32 v11, 0xffff0000, v36
	v_fmac_f32_e32 v10, v12, v32
	v_fmac_f32_e32 v11, v13, v14
	v_lshlrev_b32_e32 v17, 16, v40
	v_and_b32_e32 v40, 0xffff0000, v40
	v_add_f32_e32 v184, v184, v10
	v_add_f32_e32 v185, v185, v11
	v_mul_f32_e32 v184, v184, v17
	v_mul_f32_e32 v185, v185, v40
	v_cvt_pk_bf16_f32 v40, v184, v185
	v_lshlrev_b32_e32 v12, 16, v35
	v_and_b32_e32 v13, 0xffff0000, v35
	v_fmac_f32_e32 v12, v10, v31
	v_fmac_f32_e32 v13, v11, v7
	v_lshlrev_b32_e32 v17, 16, v39
	v_and_b32_e32 v39, 0xffff0000, v39
	v_add_f32_e32 v182, v182, v12
	v_add_f32_e32 v183, v183, v13
	v_mul_f32_e32 v182, v182, v17
	v_mul_f32_e32 v183, v183, v39
	v_cvt_pk_bf16_f32 v39, v182, v183
	v_lshlrev_b32_e32 v10, 16, v34
	v_and_b32_e32 v11, 0xffff0000, v34
	v_fmac_f32_e32 v10, v12, v30
	v_fmac_f32_e32 v11, v13, v6
	v_lshlrev_b32_e32 v17, 16, v38
	v_and_b32_e32 v38, 0xffff0000, v38
	v_add_f32_e32 v180, v180, v10
	v_add_f32_e32 v181, v181, v11
	v_mul_f32_e32 v180, v180, v17
	v_mul_f32_e32 v181, v181, v38
	v_cvt_pk_bf16_f32 v38, v180, v181
	s_nop 1
	v_permlane16_swap_b32_e32 v38, v39
	v_permlane16_swap_b32_e32 v40, v41
	s_nop 1
	v_permlane32_swap_b32_e32 v38, v40
	v_permlane32_swap_b32_e32 v39, v41
	global_store_dwordx4 v232, v[38:41], s[80:81]
	v_add_u32_e32 v232, 0xffffe000, v232
	global_load_dwordx4 v[30:33], v231, s[82:83] nt
	global_load_dwordx4 v[34:37], v231, s[84:85] nt
	global_load_dwordx4 v[38:41], v231, s[78:79] nt
	v_add_u32_e32 v231, 0xffffe000, v231
	s_waitcnt vmcnt(35)
	v_permlane16_swap_b32_e32 v42, v43
	v_permlane16_swap_b32_e32 v44, v45
	v_permlane16_swap_b32_e32 v46, v47
	v_permlane16_swap_b32_e32 v48, v49
	v_permlane16_swap_b32_e32 v50, v51
	v_permlane16_swap_b32_e32 v52, v53
	v_permlane32_swap_b32_e32 v42, v44
	v_permlane32_swap_b32_e32 v43, v45
	v_permlane32_swap_b32_e32 v46, v48
	v_permlane32_swap_b32_e32 v47, v49
	v_permlane32_swap_b32_e32 v50, v52
	v_permlane32_swap_b32_e32 v51, v53
	v_and_b32_e32 v6, 0xffff0000, v42
	v_lshlrev_b32_e32 v42, 16, v42
	v_and_b32_e32 v7, 0xffff0000, v43
	v_lshlrev_b32_e32 v43, 16, v43
	v_and_b32_e32 v14, 0xffff0000, v44
	v_lshlrev_b32_e32 v44, 16, v44
	v_and_b32_e32 v15, 0xffff0000, v45
	v_lshlrev_b32_e32 v45, 16, v45
	v_mul_f32_e32 v42, 0x3fb8aa3b, v42
	v_mul_f32_e32 v6, 0x3fb8aa3b, v6
	v_mul_f32_e32 v43, 0x3fb8aa3b, v43
	v_mul_f32_e32 v7, 0x3fb8aa3b, v7
	v_mul_f32_e32 v44, 0x3fb8aa3b, v44
	v_mul_f32_e32 v14, 0x3fb8aa3b, v14
	v_mul_f32_e32 v45, 0x3fb8aa3b, v45
	v_mul_f32_e32 v15, 0x3fb8aa3b, v15
	v_exp_f32_e32 v42, v42
	v_exp_f32_e32 v6, v6
	v_exp_f32_e32 v43, v43
	v_exp_f32_e32 v7, v7
	v_exp_f32_e32 v44, v44
	v_exp_f32_e32 v14, v14
	v_exp_f32_e32 v45, v45
	v_exp_f32_e32 v15, v15
	v_lshlrev_b32_e32 v12, 16, v49
	v_and_b32_e32 v13, 0xffff0000, v49
	v_fmac_f32_e32 v12, v10, v45
	v_fmac_f32_e32 v13, v11, v15
	v_lshlrev_b32_e32 v17, 16, v53
	v_and_b32_e32 v53, 0xffff0000, v53
	v_add_f32_e32 v178, v178, v12
	v_add_f32_e32 v179, v179, v13
	v_mul_f32_e32 v178, v178, v17
	v_mul_f32_e32 v179, v179, v53
	v_cvt_pk_bf16_f32 v53, v178, v179
	v_lshlrev_b32_e32 v10, 16, v48
	v_and_b32_e32 v11, 0xffff0000, v48
	v_fmac_f32_e32 v10, v12, v44
	v_fmac_f32_e32 v11, v13, v14
	v_lshlrev_b32_e32 v17, 16, v52
	v_and_b32_e32 v52, 0xffff0000, v52
	v_add_f32_e32 v176, v176, v10
	v_add_f32_e32 v177, v177, v11
	v_mul_f32_e32 v176, v176, v17
	v_mul_f32_e32 v177, v177, v52
	v_cvt_pk_bf16_f32 v52, v176, v177
	v_lshlrev_b32_e32 v12, 16, v47
	v_and_b32_e32 v13, 0xffff0000, v47
	v_fmac_f32_e32 v12, v10, v43
	v_fmac_f32_e32 v13, v11, v7
	v_lshlrev_b32_e32 v17, 16, v51
	v_and_b32_e32 v51, 0xffff0000, v51
	v_add_f32_e32 v174, v174, v12
	v_add_f32_e32 v175, v175, v13
	v_mul_f32_e32 v174, v174, v17
	v_mul_f32_e32 v175, v175, v51
	v_cvt_pk_bf16_f32 v51, v174, v175
	v_lshlrev_b32_e32 v10, 16, v46
	v_and_b32_e32 v11, 0xffff0000, v46
	v_fmac_f32_e32 v10, v12, v42
	v_fmac_f32_e32 v11, v13, v6
	v_lshlrev_b32_e32 v17, 16, v50
	v_and_b32_e32 v50, 0xffff0000, v50
	v_add_f32_e32 v172, v172, v10
	v_add_f32_e32 v173, v173, v11
	v_mul_f32_e32 v172, v172, v17
	v_mul_f32_e32 v173, v173, v50
	v_cvt_pk_bf16_f32 v50, v172, v173
	s_nop 1
	v_permlane16_swap_b32_e32 v50, v51
	v_permlane16_swap_b32_e32 v52, v53
	s_nop 1
	v_permlane32_swap_b32_e32 v50, v52
	v_permlane32_swap_b32_e32 v51, v53
	global_store_dwordx4 v232, v[50:53], s[80:81]
	v_add_u32_e32 v232, 0xffffe000, v232
	global_load_dwordx4 v[42:45], v231, s[82:83] nt
	global_load_dwordx4 v[46:49], v231, s[84:85] nt
	global_load_dwordx4 v[50:53], v231, s[78:79] nt
	v_add_u32_e32 v231, 0xffffe000, v231
	s_waitcnt vmcnt(36)
; __device__ __forceinline__ unsigned cvt_pk_bf16(float lo, float hi) { unsigned r; asm("v_cvt_pk_bf16_f32 %0, %1, %2" : "=v"(r) : "v"(lo), "v"(hi)); return r; }
; __device__ __forceinline__ float bf_lo(unsigned w) { return __uint_as_float(w << 16); }
; __device__ __forceinline__ float bf_hi(unsigned w) { return __uint_as_float(w & 0xffff0000u); }
; __device__ __forceinline__ void scan_s3(CTXA) {
;     ...
;         for (int g = 0; g < 4; ++g) { unsigned wl[16], wb[16], wg[16];
; #pragma unroll
;             for (int q = 0; q < 16; ++q) { const int t = 63 - (g * 16 + q); wl[q] = __builtin_nontemporal_load(la1 + (size_t)t * (D / 2)); wb[q] = __builtin_nontemporal_load(bb1 + (size_t)t * (D / 2)); wg[q] = __builtin_nontemporal_load(gg + (size_t)t * (D / 2)); }
; #pragma unroll
;             for (int q = 0; q < 16; ++q) { const int t = 63 - (g * 16 + q); hb0 = __expf(bf_lo(wl[q])) * hb0 + bf_lo(wb[q]); hb1 = __expf(bf_hi(wl[q])) * hb1 + bf_hi(wb[q]);
;                 yy[(size_t)t * (D / 2)] = cvt_pk_bf16((fv0[t] + hb0) * bf_lo(wg[q]), (fv1[t] + hb1) * bf_hi(wg[q])); } }
	v_permlane16_swap_b32_e32 v54, v55
	v_permlane16_swap_b32_e32 v56, v57
	v_permlane16_swap_b32_e32 v58, v59
	v_permlane16_swap_b32_e32 v60, v61
	v_permlane16_swap_b32_e32 v62, v63
	v_permlane16_swap_b32_e32 v64, v65
	v_permlane32_swap_b32_e32 v54, v56
	v_permlane32_swap_b32_e32 v55, v57
	v_permlane32_swap_b32_e32 v58, v60
	v_permlane32_swap_b32_e32 v59, v61
	v_permlane32_swap_b32_e32 v62, v64
	v_permlane32_swap_b32_e32 v63, v65
	v_and_b32_e32 v6, 0xffff0000, v54
	v_lshlrev_b32_e32 v54, 16, v54
	v_and_b32_e32 v7, 0xffff0000, v55
	v_lshlrev_b32_e32 v55, 16, v55
	v_and_b32_e32 v14, 0xffff0000, v56
	v_lshlrev_b32_e32 v56, 16, v56
	v_and_b32_e32 v15, 0xffff0000, v57
	v_lshlrev_b32_e32 v57, 16, v57
	v_mul_f32_e32 v54, 0x3fb8aa3b, v54
	v_mul_f32_e32 v6, 0x3fb8aa3b, v6
	v_mul_f32_e32 v55, 0x3fb8aa3b, v55
	v_mul_f32_e32 v7, 0x3fb8aa3b, v7
	v_mul_f32_e32 v56, 0x3fb8aa3b, v56
	v_mul_f32_e32 v14, 0x3fb8aa3b, v14
	v_mul_f32_e32 v57, 0x3fb8aa3b, v57
	v_mul_f32_e32 v15, 0x3fb8aa3b, v15
	v_exp_f32_e32 v54, v54
	v_exp_f32_e32 v6, v6
	v_exp_f32_e32 v55, v55
	v_exp_f32_e32 v7, v7
	v_exp_f32_e32 v56, v56
	v_exp_f32_e32 v14, v14
	v_exp_f32_e32 v57, v57
	v_exp_f32_e32 v15, v15
	v_lshlrev_b32_e32 v12, 16, v61
	v_and_b32_e32 v13, 0xffff0000, v61
	v_fmac_f32_e32 v12, v10, v57
	v_fmac_f32_e32 v13, v11, v15
	v_lshlrev_b32_e32 v17, 16, v65
	v_and_b32_e32 v65, 0xffff0000, v65
	v_add_f32_e32 v170, v170, v12
	v_add_f32_e32 v171, v171, v13
	v_mul_f32_e32 v170, v170, v17
	v_mul_f32_e32 v171, v171, v65
	v_cvt_pk_bf16_f32 v65, v170, v171
	v_lshlrev_b32_e32 v10, 16, v60
	v_and_b32_e32 v11, 0xffff0000, v60
	v_fmac_f32_e32 v10, v12, v56
	v_fmac_f32_e32 v11, v13, v14
	v_lshlrev_b32_e32 v17, 16, v64
	v_and_b32_e32 v64, 0xffff0000, v64
	v_add_f32_e32 v168, v168, v10
	v_add_f32_e32 v169, v169, v11
	v_mul_f32_e32 v168, v168, v17
	v_mul_f32_e32 v169, v169, v64
	v_cvt_pk_bf16_f32 v64, v168, v169
	v_lshlrev_b32_e32 v12, 16, v59
	v_and_b32_e32 v13, 0xffff0000, v59
	v_fmac_f32_e32 v12, v10, v55
	v_fmac_f32_e32 v13, v11, v7
	v_lshlrev_b32_e32 v17, 16, v63
	v_and_b32_e32 v63, 0xffff0000, v63
	v_add_f32_e32 v166, v166, v12
	v_add_f32_e32 v167, v167, v13
	v_mul_f32_e32 v166, v166, v17
	v_mul_f32_e32 v167, v167, v63
	v_cvt_pk_bf16_f32 v63, v166, v167
	v_lshlrev_b32_e32 v10, 16, v58
	v_and_b32_e32 v11, 0xffff0000, v58
	v_fmac_f32_e32 v10, v12, v54
	v_fmac_f32_e32 v11, v13, v6
	v_lshlrev_b32_e32 v17, 16, v62
	v_and_b32_e32 v62, 0xffff0000, v62
	v_add_f32_e32 v164, v164, v10
	v_add_f32_e32 v165, v165, v11
	v_mul_f32_e32 v164, v164, v17
	v_mul_f32_e32 v165, v165, v62
	v_cvt_pk_bf16_f32 v62, v164, v165
	s_nop 1
	v_permlane16_swap_b32_e32 v62, v63
	v_permlane16_swap_b32_e32 v64, v65
	s_nop 1
	v_permlane32_swap_b32_e32 v62, v64
	v_permlane32_swap_b32_e32 v63, v65
	global_store_dwordx4 v232, v[62:65], s[80:81]
	v_add_u32_e32 v232, 0xffffe000, v232
	global_load_dwordx4 v[54:57], v231, s[82:83] nt
	global_load_dwordx4 v[58:61], v231, s[84:85] nt
	global_load_dwordx4 v[62:65], v231, s[78:79] nt
	v_add_u32_e32 v231, 0xffffe000, v231
	s_waitcnt vmcnt(12)
	v_permlane16_swap_b32_e32 v18, v19
	v_permlane16_swap_b32_e32 v20, v21
	v_permlane16_swap_b32_e32 v22, v23
	v_permlane16_swap_b32_e32 v24, v25
	v_permlane16_swap_b32_e32 v26, v27
	v_permlane16_swap_b32_e32 v28, v29
	v_permlane32_swap_b32_e32 v18, v20
	v_permlane32_swap_b32_e32 v19, v21
	v_permlane32_swap_b32_e32 v22, v24
	v_permlane32_swap_b32_e32 v23, v25
	v_permlane32_swap_b32_e32 v26, v28
	v_permlane32_swap_b32_e32 v27, v29
	v_and_b32_e32 v6, 0xffff0000, v18
	v_lshlrev_b32_e32 v18, 16, v18
	v_and_b32_e32 v7, 0xffff0000, v19
	v_lshlrev_b32_e32 v19, 16, v19
	v_and_b32_e32 v14, 0xffff0000, v20
	v_lshlrev_b32_e32 v20, 16, v20
	v_and_b32_e32 v15, 0xffff0000, v21
	v_lshlrev_b32_e32 v21, 16, v21
	v_mul_f32_e32 v18, 0x3fb8aa3b, v18
	v_mul_f32_e32 v6, 0x3fb8aa3b, v6
	v_mul_f32_e32 v19, 0x3fb8aa3b, v19
	v_mul_f32_e32 v7, 0x3fb8aa3b, v7
	v_mul_f32_e32 v20, 0x3fb8aa3b, v20
	v_mul_f32_e32 v14, 0x3fb8aa3b, v14
	v_mul_f32_e32 v21, 0x3fb8aa3b, v21
	v_mul_f32_e32 v15, 0x3fb8aa3b, v15
	v_exp_f32_e32 v18, v18
	v_exp_f32_e32 v6, v6
	v_exp_f32_e32 v19, v19
	v_exp_f32_e32 v7, v7
	v_exp_f32_e32 v20, v20
	v_exp_f32_e32 v14, v14
	v_exp_f32_e32 v21, v21
	v_exp_f32_e32 v15, v15
	v_lshlrev_b32_e32 v12, 16, v25
	v_and_b32_e32 v13, 0xffff0000, v25
	v_fmac_f32_e32 v12, v10, v21
	v_fmac_f32_e32 v13, v11, v15
	v_lshlrev_b32_e32 v17, 16, v29
	v_and_b32_e32 v29, 0xffff0000, v29
	v_add_f32_e32 v162, v162, v12
	v_add_f32_e32 v163, v163, v13
	v_mul_f32_e32 v162, v162, v17
	v_mul_f32_e32 v163, v163, v29
	v_cvt_pk_bf16_f32 v29, v162, v163
	v_lshlrev_b32_e32 v10, 16, v24
	v_and_b32_e32 v11, 0xffff0000, v24
	v_fmac_f32_e32 v10, v12, v20
	v_fmac_f32_e32 v11, v13, v14
	v_lshlrev_b32_e32 v17, 16, v28
	v_and_b32_e32 v28, 0xffff0000, v28
	v_add_f32_e32 v160, v160, v10
	v_add_f32_e32 v161, v161, v11
	v_mul_f32_e32 v160, v160, v17
	v_mul_f32_e32 v161, v161, v28
	v_cvt_pk_bf16_f32 v28, v160, v161
	v_lshlrev_b32_e32 v12, 16, v23
	v_and_b32_e32 v13, 0xffff0000, v23
	v_fmac_f32_e32 v12, v10, v19
	v_fmac_f32_e32 v13, v11, v7
	v_lshlrev_b32_e32 v17, 16, v27
	v_and_b32_e32 v27, 0xffff0000, v27
	v_add_f32_e32 v158, v158, v12
	v_add_f32_e32 v159, v159, v13
	v_mul_f32_e32 v158, v158, v17
	v_mul_f32_e32 v159, v159, v27
	v_cvt_pk_bf16_f32 v27, v158, v159
	v_lshlrev_b32_e32 v10, 16, v22
	v_and_b32_e32 v11, 0xffff0000, v22
	v_fmac_f32_e32 v10, v12, v18
	v_fmac_f32_e32 v11, v13, v6
	v_lshlrev_b32_e32 v17, 16, v26
	v_and_b32_e32 v26, 0xffff0000, v26
	v_add_f32_e32 v156, v156, v10
	v_add_f32_e32 v157, v157, v11
	v_mul_f32_e32 v156, v156, v17
	v_mul_f32_e32 v157, v157, v26
	v_cvt_pk_bf16_f32 v26, v156, v157
	s_nop 1
	v_permlane16_swap_b32_e32 v26, v27
	v_permlane16_swap_b32_e32 v28, v29
	s_nop 1
	v_permlane32_swap_b32_e32 v26, v28
	v_permlane32_swap_b32_e32 v27, v29
	global_store_dwordx4 v232, v[26:29], s[80:81]
	v_add_u32_e32 v232, 0xffffe000, v232
	global_load_dwordx4 v[18:21], v231, s[82:83] nt
	global_load_dwordx4 v[22:25], v231, s[84:85] nt
	global_load_dwordx4 v[26:29], v231, s[78:79] nt
	v_add_u32_e32 v231, 0xffffe000, v231
	s_waitcnt vmcnt(12)
; __device__ __forceinline__ unsigned cvt_pk_bf16(float lo, float hi) { unsigned r; asm("v_cvt_pk_bf16_f32 %0, %1, %2" : "=v"(r) : "v"(lo), "v"(hi)); return r; }
; __device__ __forceinline__ float bf_lo(unsigned w) { return __uint_as_float(w << 16); }
; __device__ __forceinline__ float bf_hi(unsigned w) { return __uint_as_float(w & 0xffff0000u); }
; __device__ __forceinline__ void scan_s3(CTXA) {
;     ...
;         for (int g = 0; g < 4; ++g) { unsigned wl[16], wb[16], wg[16];
; #pragma unroll
;             for (int q = 0; q < 16; ++q) { const int t = 63 - (g * 16 + q); wl[q] = __builtin_nontemporal_load(la1 + (size_t)t * (D / 2)); wb[q] = __builtin_nontemporal_load(bb1 + (size_t)t * (D / 2)); wg[q] = __builtin_nontemporal_load(gg + (size_t)t * (D / 2)); }
; #pragma unroll
;             for (int q = 0; q < 16; ++q) { const int t = 63 - (g * 16 + q); hb0 = __expf(bf_lo(wl[q])) * hb0 + bf_lo(wb[q]); hb1 = __expf(bf_hi(wl[q])) * hb1 + bf_hi(wb[q]);
;                 yy[(size_t)t * (D / 2)] = cvt_pk_bf16((fv0[t] + hb0) * bf_lo(wg[q]), (fv1[t] + hb1) * bf_hi(wg[q])); } }
	v_permlane16_swap_b32_e32 v30, v31
	v_permlane16_swap_b32_e32 v32, v33
	v_permlane16_swap_b32_e32 v34, v35
	v_permlane16_swap_b32_e32 v36, v37
	v_permlane16_swap_b32_e32 v38, v39
	v_permlane16_swap_b32_e32 v40, v41
	v_permlane32_swap_b32_e32 v30, v32
	v_permlane32_swap_b32_e32 v31, v33
	v_permlane32_swap_b32_e32 v34, v36
	v_permlane32_swap_b32_e32 v35, v37
	v_permlane32_swap_b32_e32 v38, v40
	v_permlane32_swap_b32_e32 v39, v41
	v_and_b32_e32 v6, 0xffff0000, v30
	v_lshlrev_b32_e32 v30, 16, v30
	v_and_b32_e32 v7, 0xffff0000, v31
	v_lshlrev_b32_e32 v31, 16, v31
	v_and_b32_e32 v14, 0xffff0000, v32
	v_lshlrev_b32_e32 v32, 16, v32
	v_and_b32_e32 v15, 0xffff0000, v33
	v_lshlrev_b32_e32 v33, 16, v33
	v_mul_f32_e32 v30, 0x3fb8aa3b, v30
	v_mul_f32_e32 v6, 0x3fb8aa3b, v6
	v_mul_f32_e32 v31, 0x3fb8aa3b, v31
	v_mul_f32_e32 v7, 0x3fb8aa3b, v7
	v_mul_f32_e32 v32, 0x3fb8aa3b, v32
	v_mul_f32_e32 v14, 0x3fb8aa3b, v14
	v_mul_f32_e32 v33, 0x3fb8aa3b, v33
	v_mul_f32_e32 v15, 0x3fb8aa3b, v15
	v_exp_f32_e32 v30, v30
	v_exp_f32_e32 v6, v6
	v_exp_f32_e32 v31, v31
	v_exp_f32_e32 v7, v7
	v_exp_f32_e32 v32, v32
	v_exp_f32_e32 v14, v14
	v_exp_f32_e32 v33, v33
	v_exp_f32_e32 v15, v15
	v_lshlrev_b32_e32 v12, 16, v37
	v_and_b32_e32 v13, 0xffff0000, v37
	v_fmac_f32_e32 v12, v10, v33
	v_fmac_f32_e32 v13, v11, v15
	v_lshlrev_b32_e32 v17, 16, v41
	v_and_b32_e32 v41, 0xffff0000, v41
	v_add_f32_e32 v154, v154, v12
	v_add_f32_e32 v155, v155, v13
	v_mul_f32_e32 v154, v154, v17
	v_mul_f32_e32 v155, v155, v41
	v_cvt_pk_bf16_f32 v41, v154, v155
	v_lshlrev_b32_e32 v10, 16, v36
	v_and_b32_e32 v11, 0xffff0000, v36
	v_fmac_f32_e32 v10, v12, v32
	v_fmac_f32_e32 v11, v13, v14
	v_lshlrev_b32_e32 v17, 16, v40
	v_and_b32_e32 v40, 0xffff0000, v40
	v_add_f32_e32 v152, v152, v10
	v_add_f32_e32 v153, v153, v11
	v_mul_f32_e32 v152, v152, v17
	v_mul_f32_e32 v153, v153, v40
	v_cvt_pk_bf16_f32 v40, v152, v153
	v_lshlrev_b32_e32 v12, 16, v35
	v_and_b32_e32 v13, 0xffff0000, v35
	v_fmac_f32_e32 v12, v10, v31
	v_fmac_f32_e32 v13, v11, v7
	v_lshlrev_b32_e32 v17, 16, v39
	v_and_b32_e32 v39, 0xffff0000, v39
	v_add_f32_e32 v150, v150, v12
	v_add_f32_e32 v151, v151, v13
	v_mul_f32_e32 v150, v150, v17
	v_mul_f32_e32 v151, v151, v39
	v_cvt_pk_bf16_f32 v39, v150, v151
	v_lshlrev_b32_e32 v10, 16, v34
	v_and_b32_e32 v11, 0xffff0000, v34
	v_fmac_f32_e32 v10, v12, v30
	v_fmac_f32_e32 v11, v13, v6
	v_lshlrev_b32_e32 v17, 16, v38
	v_and_b32_e32 v38, 0xffff0000, v38
	v_add_f32_e32 v148, v148, v10
	v_add_f32_e32 v149, v149, v11
	v_mul_f32_e32 v148, v148, v17
	v_mul_f32_e32 v149, v149, v38
	v_cvt_pk_bf16_f32 v38, v148, v149
	s_nop 1
	v_permlane16_swap_b32_e32 v38, v39
	v_permlane16_swap_b32_e32 v40, v41
	s_nop 1
	v_permlane32_swap_b32_e32 v38, v40
	v_permlane32_swap_b32_e32 v39, v41
	global_store_dwordx4 v232, v[38:41], s[80:81]
	v_add_u32_e32 v232, 0xffffe000, v232
	global_load_dwordx4 v[30:33], v231, s[82:83] nt
	global_load_dwordx4 v[34:37], v231, s[84:85] nt
	global_load_dwordx4 v[38:41], v231, s[78:79] nt
	v_add_u32_e32 v231, 0xffffe000, v231
	s_waitcnt vmcnt(12)
	v_permlane16_swap_b32_e32 v42, v43
	v_permlane16_swap_b32_e32 v44, v45
	v_permlane16_swap_b32_e32 v46, v47
	v_permlane16_swap_b32_e32 v48, v49
	v_permlane16_swap_b32_e32 v50, v51
	v_permlane16_swap_b32_e32 v52, v53
	v_permlane32_swap_b32_e32 v42, v44
	v_permlane32_swap_b32_e32 v43, v45
	v_permlane32_swap_b32_e32 v46, v48
	v_permlane32_swap_b32_e32 v47, v49
	v_permlane32_swap_b32_e32 v50, v52
	v_permlane32_swap_b32_e32 v51, v53
	v_and_b32_e32 v6, 0xffff0000, v42
	v_lshlrev_b32_e32 v42, 16, v42
	v_and_b32_e32 v7, 0xffff0000, v43
	v_lshlrev_b32_e32 v43, 16, v43
	v_and_b32_e32 v14, 0xffff0000, v44
	v_lshlrev_b32_e32 v44, 16, v44
	v_and_b32_e32 v15, 0xffff0000, v45
	v_lshlrev_b32_e32 v45, 16, v45
	v_mul_f32_e32 v42, 0x3fb8aa3b, v42
	v_mul_f32_e32 v6, 0x3fb8aa3b, v6
	v_mul_f32_e32 v43, 0x3fb8aa3b, v43
	v_mul_f32_e32 v7, 0x3fb8aa3b, v7
	v_mul_f32_e32 v44, 0x3fb8aa3b, v44
	v_mul_f32_e32 v14, 0x3fb8aa3b, v14
	v_mul_f32_e32 v45, 0x3fb8aa3b, v45
	v_mul_f32_e32 v15, 0x3fb8aa3b, v15
	v_exp_f32_e32 v42, v42
	v_exp_f32_e32 v6, v6
	v_exp_f32_e32 v43, v43
	v_exp_f32_e32 v7, v7
	v_exp_f32_e32 v44, v44
	v_exp_f32_e32 v14, v14
	v_exp_f32_e32 v45, v45
	v_exp_f32_e32 v15, v15
	v_lshlrev_b32_e32 v12, 16, v49
	v_and_b32_e32 v13, 0xffff0000, v49
	v_fmac_f32_e32 v12, v10, v45
	v_fmac_f32_e32 v13, v11, v15
	v_lshlrev_b32_e32 v17, 16, v53
	v_and_b32_e32 v53, 0xffff0000, v53
	v_add_f32_e32 v146, v146, v12
	v_add_f32_e32 v147, v147, v13
	v_mul_f32_e32 v146, v146, v17
	v_mul_f32_e32 v147, v147, v53
	v_cvt_pk_bf16_f32 v53, v146, v147
	v_lshlrev_b32_e32 v10, 16, v48
	v_and_b32_e32 v11, 0xffff0000, v48
	v_fmac_f32_e32 v10, v12, v44
	v_fmac_f32_e32 v11, v13, v14
	v_lshlrev_b32_e32 v17, 16, v52
	v_and_b32_e32 v52, 0xffff0000, v52
	v_add_f32_e32 v144, v144, v10
	v_add_f32_e32 v145, v145, v11
	v_mul_f32_e32 v144, v144, v17
	v_mul_f32_e32 v145, v145, v52
	v_cvt_pk_bf16_f32 v52, v144, v145
	v_lshlrev_b32_e32 v12, 16, v47
	v_and_b32_e32 v13, 0xffff0000, v47
	v_fmac_f32_e32 v12, v10, v43
	v_fmac_f32_e32 v13, v11, v7
	v_lshlrev_b32_e32 v17, 16, v51
	v_and_b32_e32 v51, 0xffff0000, v51
	v_add_f32_e32 v142, v142, v12
	v_add_f32_e32 v143, v143, v13
	v_mul_f32_e32 v142, v142, v17
	v_mul_f32_e32 v143, v143, v51
	v_cvt_pk_bf16_f32 v51, v142, v143
	v_lshlrev_b32_e32 v10, 16, v46
	v_and_b32_e32 v11, 0xffff0000, v46
	v_fmac_f32_e32 v10, v12, v42
	v_fmac_f32_e32 v11, v13, v6
	v_lshlrev_b32_e32 v17, 16, v50
	v_and_b32_e32 v50, 0xffff0000, v50
	v_add_f32_e32 v140, v140, v10
	v_add_f32_e32 v141, v141, v11
	v_mul_f32_e32 v140, v140, v17
	v_mul_f32_e32 v141, v141, v50
	v_cvt_pk_bf16_f32 v50, v140, v141
	s_nop 1
	v_permlane16_swap_b32_e32 v50, v51
	v_permlane16_swap_b32_e32 v52, v53
	s_nop 1
	v_permlane32_swap_b32_e32 v50, v52
	v_permlane32_swap_b32_e32 v51, v53
	global_store_dwordx4 v232, v[50:53], s[80:81]
	v_add_u32_e32 v232, 0xffffe000, v232
	global_load_dwordx4 v[42:45], v231, s[82:83] nt
	global_load_dwordx4 v[46:49], v231, s[84:85] nt
	global_load_dwordx4 v[50:53], v231, s[78:79] nt
	v_add_u32_e32 v231, 0xffffe000, v231
	s_waitcnt vmcnt(12)
; __device__ __forceinline__ unsigned cvt_pk_bf16(float lo, float hi) { unsigned r; asm("v_cvt_pk_bf16_f32 %0, %1, %2" : "=v"(r) : "v"(lo), "v"(hi)); return r; }
; __device__ __forceinline__ float bf_lo(unsigned w) { return __uint_as_float(w << 16); }
; __device__ __forceinline__ float bf_hi(unsigned w) { return __uint_as_float(w & 0xffff0000u); }
; __device__ __forceinline__ void scan_s3(CTXA) {
;     ...
;         for (int g = 0; g < 4; ++g) { unsigned wl[16], wb[16], wg[16];
; #pragma unroll
;             for (int q = 0; q < 16; ++q) { const int t = 63 - (g * 16 + q); wl[q] = __builtin_nontemporal_load(la1 + (size_t)t * (D / 2)); wb[q] = __builtin_nontemporal_load(bb1 + (size_t)t * (D / 2)); wg[q] = __builtin_nontemporal_load(gg + (size_t)t * (D / 2)); }
; #pragma unroll
;             for (int q = 0; q < 16; ++q) { const int t = 63 - (g * 16 + q); hb0 = __expf(bf_lo(wl[q])) * hb0 + bf_lo(wb[q]); hb1 = __expf(bf_hi(wl[q])) * hb1 + bf_hi(wb[q]);
;                 yy[(size_t)t * (D / 2)] = cvt_pk_bf16((fv0[t] + hb0) * bf_lo(wg[q]), (fv1[t] + hb1) * bf_hi(wg[q])); } }
	v_permlane16_swap_b32_e32 v54, v55
	v_permlane16_swap_b32_e32 v56, v57
	v_permlane16_swap_b32_e32 v58, v59
	v_permlane16_swap_b32_e32 v60, v61
	v_permlane16_swap_b32_e32 v62, v63
	v_permlane16_swap_b32_e32 v64, v65
	v_permlane32_swap_b32_e32 v54, v56
	v_permlane32_swap_b32_e32 v55, v57
	v_permlane32_swap_b32_e32 v58, v60
	v_permlane32_swap_b32_e32 v59, v61
	v_permlane32_swap_b32_e32 v62, v64
	v_permlane32_swap_b32_e32 v63, v65
	v_and_b32_e32 v6, 0xffff0000, v54
	v_lshlrev_b32_e32 v54, 16, v54
	v_and_b32_e32 v7, 0xffff0000, v55
	v_lshlrev_b32_e32 v55, 16, v55
	v_and_b32_e32 v14, 0xffff0000, v56
	v_lshlrev_b32_e32 v56, 16, v56
	v_and_b32_e32 v15, 0xffff0000, v57
	v_lshlrev_b32_e32 v57, 16, v57
	v_mul_f32_e32 v54, 0x3fb8aa3b, v54
	v_mul_f32_e32 v6, 0x3fb8aa3b, v6
	v_mul_f32_e32 v55, 0x3fb8aa3b, v55
	v_mul_f32_e32 v7, 0x3fb8aa3b, v7
	v_mul_f32_e32 v56, 0x3fb8aa3b, v56
	v_mul_f32_e32 v14, 0x3fb8aa3b, v14
	v_mul_f32_e32 v57, 0x3fb8aa3b, v57
	v_mul_f32_e32 v15, 0x3fb8aa3b, v15
	v_exp_f32_e32 v54, v54
	v_exp_f32_e32 v6, v6
	v_exp_f32_e32 v55, v55
	v_exp_f32_e32 v7, v7
	v_exp_f32_e32 v56, v56
	v_exp_f32_e32 v14, v14
	v_exp_f32_e32 v57, v57
	v_exp_f32_e32 v15, v15
	v_lshlrev_b32_e32 v12, 16, v61
	v_and_b32_e32 v13, 0xffff0000, v61
	v_fmac_f32_e32 v12, v10, v57
	v_fmac_f32_e32 v13, v11, v15
	v_lshlrev_b32_e32 v17, 16, v65
	v_and_b32_e32 v65, 0xffff0000, v65
	v_add_f32_e32 v138, v138, v12
	v_add_f32_e32 v139, v139, v13
	v_mul_f32_e32 v138, v138, v17
	v_mul_f32_e32 v139, v139, v65
	v_cvt_pk_bf16_f32 v65, v138, v139
	v_lshlrev_b32_e32 v10, 16, v60
	v_and_b32_e32 v11, 0xffff0000, v60
	v_fmac_f32_e32 v10, v12, v56
	v_fmac_f32_e32 v11, v13, v14
	v_lshlrev_b32_e32 v17, 16, v64
	v_and_b32_e32 v64, 0xffff0000, v64
	v_add_f32_e32 v136, v136, v10
	v_add_f32_e32 v137, v137, v11
	v_mul_f32_e32 v136, v136, v17
	v_mul_f32_e32 v137, v137, v64
	v_cvt_pk_bf16_f32 v64, v136, v137
	v_lshlrev_b32_e32 v12, 16, v59
	v_and_b32_e32 v13, 0xffff0000, v59
	v_fmac_f32_e32 v12, v10, v55
	v_fmac_f32_e32 v13, v11, v7
	v_lshlrev_b32_e32 v17, 16, v63
	v_and_b32_e32 v63, 0xffff0000, v63
	v_add_f32_e32 v134, v134, v12
	v_add_f32_e32 v135, v135, v13
	v_mul_f32_e32 v134, v134, v17
	v_mul_f32_e32 v135, v135, v63
	v_cvt_pk_bf16_f32 v63, v134, v135
	v_lshlrev_b32_e32 v10, 16, v58
	v_and_b32_e32 v11, 0xffff0000, v58
	v_fmac_f32_e32 v10, v12, v54
	v_fmac_f32_e32 v11, v13, v6
	v_lshlrev_b32_e32 v17, 16, v62
	v_and_b32_e32 v62, 0xffff0000, v62
	v_add_f32_e32 v132, v132, v10
	v_add_f32_e32 v133, v133, v11
	v_mul_f32_e32 v132, v132, v17
	v_mul_f32_e32 v133, v133, v62
	v_cvt_pk_bf16_f32 v62, v132, v133
	s_nop 1
	v_permlane16_swap_b32_e32 v62, v63
	v_permlane16_swap_b32_e32 v64, v65
	s_nop 1
	v_permlane32_swap_b32_e32 v62, v64
	v_permlane32_swap_b32_e32 v63, v65
	global_store_dwordx4 v232, v[62:65], s[80:81]
	v_add_u32_e32 v232, 0xffffe000, v232
	global_load_dwordx4 v[54:57], v231, s[82:83] nt
	global_load_dwordx4 v[58:61], v231, s[84:85] nt
	global_load_dwordx4 v[62:65], v231, s[78:79] nt
	v_add_u32_e32 v231, 0xffffe000, v231
	s_waitcnt vmcnt(12)
	v_permlane16_swap_b32_e32 v18, v19
	v_permlane16_swap_b32_e32 v20, v21
	v_permlane16_swap_b32_e32 v22, v23
	v_permlane16_swap_b32_e32 v24, v25
	v_permlane16_swap_b32_e32 v26, v27
	v_permlane16_swap_b32_e32 v28, v29
	v_permlane32_swap_b32_e32 v18, v20
	v_permlane32_swap_b32_e32 v19, v21
	v_permlane32_swap_b32_e32 v22, v24
	v_permlane32_swap_b32_e32 v23, v25
	v_permlane32_swap_b32_e32 v26, v28
	v_permlane32_swap_b32_e32 v27, v29
	v_and_b32_e32 v6, 0xffff0000, v18
	v_lshlrev_b32_e32 v18, 16, v18
	v_and_b32_e32 v7, 0xffff0000, v19
	v_lshlrev_b32_e32 v19, 16, v19
	v_and_b32_e32 v14, 0xffff0000, v20
	v_lshlrev_b32_e32 v20, 16, v20
	v_and_b32_e32 v15, 0xffff0000, v21
	v_lshlrev_b32_e32 v21, 16, v21
	v_mul_f32_e32 v18, 0x3fb8aa3b, v18
	v_mul_f32_e32 v6, 0x3fb8aa3b, v6
	v_mul_f32_e32 v19, 0x3fb8aa3b, v19
	v_mul_f32_e32 v7, 0x3fb8aa3b, v7
	v_mul_f32_e32 v20, 0x3fb8aa3b, v20
	v_mul_f32_e32 v14, 0x3fb8aa3b, v14
	v_mul_f32_e32 v21, 0x3fb8aa3b, v21
	v_mul_f32_e32 v15, 0x3fb8aa3b, v15
	v_exp_f32_e32 v18, v18
	v_exp_f32_e32 v6, v6
	v_exp_f32_e32 v19, v19
	v_exp_f32_e32 v7, v7
	v_exp_f32_e32 v20, v20
	v_exp_f32_e32 v14, v14
	v_exp_f32_e32 v21, v21
	v_exp_f32_e32 v15, v15
	v_lshlrev_b32_e32 v12, 16, v25
	v_and_b32_e32 v13, 0xffff0000, v25
	v_fmac_f32_e32 v12, v10, v21
	v_fmac_f32_e32 v13, v11, v15
	v_lshlrev_b32_e32 v17, 16, v29
	v_and_b32_e32 v29, 0xffff0000, v29
	v_add_f32_e32 v130, v130, v12
	v_add_f32_e32 v131, v131, v13
	v_mul_f32_e32 v130, v130, v17
	v_mul_f32_e32 v131, v131, v29
	v_cvt_pk_bf16_f32 v29, v130, v131
	v_lshlrev_b32_e32 v10, 16, v24
	v_and_b32_e32 v11, 0xffff0000, v24
	v_fmac_f32_e32 v10, v12, v20
	v_fmac_f32_e32 v11, v13, v14
	v_lshlrev_b32_e32 v17, 16, v28
	v_and_b32_e32 v28, 0xffff0000, v28
	v_add_f32_e32 v128, v128, v10
	v_add_f32_e32 v129, v129, v11
	v_mul_f32_e32 v128, v128, v17
	v_mul_f32_e32 v129, v129, v28
	v_cvt_pk_bf16_f32 v28, v128, v129
	v_lshlrev_b32_e32 v12, 16, v23
	v_and_b32_e32 v13, 0xffff0000, v23
	v_fmac_f32_e32 v12, v10, v19
	v_fmac_f32_e32 v13, v11, v7
	v_lshlrev_b32_e32 v17, 16, v27
	v_and_b32_e32 v27, 0xffff0000, v27
	v_add_f32_e32 v126, v126, v12
	v_add_f32_e32 v127, v127, v13
	v_mul_f32_e32 v126, v126, v17
	v_mul_f32_e32 v127, v127, v27
	v_cvt_pk_bf16_f32 v27, v126, v127
	v_lshlrev_b32_e32 v10, 16, v22
	v_and_b32_e32 v11, 0xffff0000, v22
	v_fmac_f32_e32 v10, v12, v18
	v_fmac_f32_e32 v11, v13, v6
	v_lshlrev_b32_e32 v17, 16, v26
	v_and_b32_e32 v26, 0xffff0000, v26
	v_add_f32_e32 v124, v124, v10
	v_add_f32_e32 v125, v125, v11
	v_mul_f32_e32 v124, v124, v17
	v_mul_f32_e32 v125, v125, v26
	v_cvt_pk_bf16_f32 v26, v124, v125
	s_nop 1
	v_permlane16_swap_b32_e32 v26, v27
	v_permlane16_swap_b32_e32 v28, v29
	s_nop 1
	v_permlane32_swap_b32_e32 v26, v28
	v_permlane32_swap_b32_e32 v27, v29
	global_store_dwordx4 v232, v[26:29], s[80:81]
	v_add_u32_e32 v232, 0xffffe000, v232
	global_load_dwordx4 v[18:21], v231, s[82:83] nt
	global_load_dwordx4 v[22:25], v231, s[84:85] nt
	global_load_dwordx4 v[26:29], v231, s[78:79] nt
	v_add_u32_e32 v231, 0xffffe000, v231
	s_waitcnt vmcnt(12)
; __device__ __forceinline__ unsigned cvt_pk_bf16(float lo, float hi) { unsigned r; asm("v_cvt_pk_bf16_f32 %0, %1, %2" : "=v"(r) : "v"(lo), "v"(hi)); return r; }
; __device__ __forceinline__ float bf_lo(unsigned w) { return __uint_as_float(w << 16); }
; __device__ __forceinline__ float bf_hi(unsigned w) { return __uint_as_float(w & 0xffff0000u); }
; __device__ __forceinline__ void scan_s3(CTXA) {
;     ...
;         for (int g = 0; g < 4; ++g) { unsigned wl[16], wb[16], wg[16];
; #pragma unroll
;             for (int q = 0; q < 16; ++q) { const int t = 63 - (g * 16 + q); wl[q] = __builtin_nontemporal_load(la1 + (size_t)t * (D / 2)); wb[q] = __builtin_nontemporal_load(bb1 + (size_t)t * (D / 2)); wg[q] = __builtin_nontemporal_load(gg + (size_t)t * (D / 2)); }
; #pragma unroll
;             for (int q = 0; q < 16; ++q) { const int t = 63 - (g * 16 + q); hb0 = __expf(bf_lo(wl[q])) * hb0 + bf_lo(wb[q]); hb1 = __expf(bf_hi(wl[q])) * hb1 + bf_hi(wb[q]);
;                 yy[(size_t)t * (D / 2)] = cvt_pk_bf16((fv0[t] + hb0) * bf_lo(wg[q]), (fv1[t] + hb1) * bf_hi(wg[q])); } }
	v_permlane16_swap_b32_e32 v30, v31
	v_permlane16_swap_b32_e32 v32, v33
	v_permlane16_swap_b32_e32 v34, v35
	v_permlane16_swap_b32_e32 v36, v37
	v_permlane16_swap_b32_e32 v38, v39
	v_permlane16_swap_b32_e32 v40, v41
	v_permlane32_swap_b32_e32 v30, v32
	v_permlane32_swap_b32_e32 v31, v33
	v_permlane32_swap_b32_e32 v34, v36
	v_permlane32_swap_b32_e32 v35, v37
	v_permlane32_swap_b32_e32 v38, v40
	v_permlane32_swap_b32_e32 v39, v41
	v_and_b32_e32 v6, 0xffff0000, v30
	v_lshlrev_b32_e32 v30, 16, v30
	v_and_b32_e32 v7, 0xffff0000, v31
	v_lshlrev_b32_e32 v31, 16, v31
	v_and_b32_e32 v14, 0xffff0000, v32
	v_lshlrev_b32_e32 v32, 16, v32
	v_and_b32_e32 v15, 0xffff0000, v33
	v_lshlrev_b32_e32 v33, 16, v33
	v_mul_f32_e32 v30, 0x3fb8aa3b, v30
	v_mul_f32_e32 v6, 0x3fb8aa3b, v6
	v_mul_f32_e32 v31, 0x3fb8aa3b, v31
	v_mul_f32_e32 v7, 0x3fb8aa3b, v7
	v_mul_f32_e32 v32, 0x3fb8aa3b, v32
	v_mul_f32_e32 v14, 0x3fb8aa3b, v14
	v_mul_f32_e32 v33, 0x3fb8aa3b, v33
	v_mul_f32_e32 v15, 0x3fb8aa3b, v15
	v_exp_f32_e32 v30, v30
	v_exp_f32_e32 v6, v6
	v_exp_f32_e32 v31, v31
	v_exp_f32_e32 v7, v7
	v_exp_f32_e32 v32, v32
	v_exp_f32_e32 v14, v14
	v_exp_f32_e32 v33, v33
	v_exp_f32_e32 v15, v15
	v_lshlrev_b32_e32 v12, 16, v37
	v_and_b32_e32 v13, 0xffff0000, v37
	v_fmac_f32_e32 v12, v10, v33
	v_fmac_f32_e32 v13, v11, v15
	v_lshlrev_b32_e32 v17, 16, v41
	v_and_b32_e32 v41, 0xffff0000, v41
	v_add_f32_e32 v122, v122, v12
	v_add_f32_e32 v123, v123, v13
	v_mul_f32_e32 v122, v122, v17
	v_mul_f32_e32 v123, v123, v41
	v_cvt_pk_bf16_f32 v41, v122, v123
	v_lshlrev_b32_e32 v10, 16, v36
	v_and_b32_e32 v11, 0xffff0000, v36
	v_fmac_f32_e32 v10, v12, v32
	v_fmac_f32_e32 v11, v13, v14
	v_lshlrev_b32_e32 v17, 16, v40
	v_and_b32_e32 v40, 0xffff0000, v40
	v_add_f32_e32 v120, v120, v10
	v_add_f32_e32 v121, v121, v11
	v_mul_f32_e32 v120, v120, v17
	v_mul_f32_e32 v121, v121, v40
	v_cvt_pk_bf16_f32 v40, v120, v121
	v_lshlrev_b32_e32 v12, 16, v35
	v_and_b32_e32 v13, 0xffff0000, v35
	v_fmac_f32_e32 v12, v10, v31
	v_fmac_f32_e32 v13, v11, v7
	v_lshlrev_b32_e32 v17, 16, v39
	v_and_b32_e32 v39, 0xffff0000, v39
	v_add_f32_e32 v118, v118, v12
	v_add_f32_e32 v119, v119, v13
	v_mul_f32_e32 v118, v118, v17
	v_mul_f32_e32 v119, v119, v39
	v_cvt_pk_bf16_f32 v39, v118, v119
	v_lshlrev_b32_e32 v10, 16, v34
	v_and_b32_e32 v11, 0xffff0000, v34
	v_fmac_f32_e32 v10, v12, v30
	v_fmac_f32_e32 v11, v13, v6
	v_lshlrev_b32_e32 v17, 16, v38
	v_and_b32_e32 v38, 0xffff0000, v38
	v_add_f32_e32 v116, v116, v10
	v_add_f32_e32 v117, v117, v11
	v_mul_f32_e32 v116, v116, v17
	v_mul_f32_e32 v117, v117, v38
	v_cvt_pk_bf16_f32 v38, v116, v117
	s_nop 1
	v_permlane16_swap_b32_e32 v38, v39
	v_permlane16_swap_b32_e32 v40, v41
	s_nop 1
	v_permlane32_swap_b32_e32 v38, v40
	v_permlane32_swap_b32_e32 v39, v41
	global_store_dwordx4 v232, v[38:41], s[80:81]
	v_add_u32_e32 v232, 0xffffe000, v232
	global_load_dwordx4 v[30:33], v231, s[82:83] nt
	global_load_dwordx4 v[34:37], v231, s[84:85] nt
	global_load_dwordx4 v[38:41], v231, s[78:79] nt
	v_add_u32_e32 v231, 0xffffe000, v231
	s_waitcnt vmcnt(12)
	v_permlane16_swap_b32_e32 v42, v43
	v_permlane16_swap_b32_e32 v44, v45
	v_permlane16_swap_b32_e32 v46, v47
	v_permlane16_swap_b32_e32 v48, v49
	v_permlane16_swap_b32_e32 v50, v51
	v_permlane16_swap_b32_e32 v52, v53
	v_permlane32_swap_b32_e32 v42, v44
	v_permlane32_swap_b32_e32 v43, v45
	v_permlane32_swap_b32_e32 v46, v48
	v_permlane32_swap_b32_e32 v47, v49
	v_permlane32_swap_b32_e32 v50, v52
	v_permlane32_swap_b32_e32 v51, v53
	v_and_b32_e32 v6, 0xffff0000, v42
	v_lshlrev_b32_e32 v42, 16, v42
	v_and_b32_e32 v7, 0xffff0000, v43
	v_lshlrev_b32_e32 v43, 16, v43
	v_and_b32_e32 v14, 0xffff0000, v44
	v_lshlrev_b32_e32 v44, 16, v44
	v_and_b32_e32 v15, 0xffff0000, v45
	v_lshlrev_b32_e32 v45, 16, v45
	v_mul_f32_e32 v42, 0x3fb8aa3b, v42
	v_mul_f32_e32 v6, 0x3fb8aa3b, v6
	v_mul_f32_e32 v43, 0x3fb8aa3b, v43
	v_mul_f32_e32 v7, 0x3fb8aa3b, v7
	v_mul_f32_e32 v44, 0x3fb8aa3b, v44
	v_mul_f32_e32 v14, 0x3fb8aa3b, v14
	v_mul_f32_e32 v45, 0x3fb8aa3b, v45
	v_mul_f32_e32 v15, 0x3fb8aa3b, v15
	v_exp_f32_e32 v42, v42
	v_exp_f32_e32 v6, v6
	v_exp_f32_e32 v43, v43
	v_exp_f32_e32 v7, v7
	v_exp_f32_e32 v44, v44
	v_exp_f32_e32 v14, v14
	v_exp_f32_e32 v45, v45
	v_exp_f32_e32 v15, v15
	v_lshlrev_b32_e32 v12, 16, v49
	v_and_b32_e32 v13, 0xffff0000, v49
	v_fmac_f32_e32 v12, v10, v45
	v_fmac_f32_e32 v13, v11, v15
	v_lshlrev_b32_e32 v17, 16, v53
	v_and_b32_e32 v53, 0xffff0000, v53
	v_add_f32_e32 v114, v114, v12
	v_add_f32_e32 v115, v115, v13
	v_mul_f32_e32 v114, v114, v17
	v_mul_f32_e32 v115, v115, v53
	v_cvt_pk_bf16_f32 v53, v114, v115
	v_lshlrev_b32_e32 v10, 16, v48
	v_and_b32_e32 v11, 0xffff0000, v48
	v_fmac_f32_e32 v10, v12, v44
	v_fmac_f32_e32 v11, v13, v14
	v_lshlrev_b32_e32 v17, 16, v52
	v_and_b32_e32 v52, 0xffff0000, v52
	v_add_f32_e32 v112, v112, v10
	v_add_f32_e32 v113, v113, v11
	v_mul_f32_e32 v112, v112, v17
	v_mul_f32_e32 v113, v113, v52
	v_cvt_pk_bf16_f32 v52, v112, v113
	v_lshlrev_b32_e32 v12, 16, v47
	v_and_b32_e32 v13, 0xffff0000, v47
	v_fmac_f32_e32 v12, v10, v43
	v_fmac_f32_e32 v13, v11, v7
	v_lshlrev_b32_e32 v17, 16, v51
	v_and_b32_e32 v51, 0xffff0000, v51
	v_add_f32_e32 v110, v110, v12
	v_add_f32_e32 v111, v111, v13
	v_mul_f32_e32 v110, v110, v17
	v_mul_f32_e32 v111, v111, v51
	v_cvt_pk_bf16_f32 v51, v110, v111
	v_lshlrev_b32_e32 v10, 16, v46
	v_and_b32_e32 v11, 0xffff0000, v46
	v_fmac_f32_e32 v10, v12, v42
	v_fmac_f32_e32 v11, v13, v6
	v_lshlrev_b32_e32 v17, 16, v50
	v_and_b32_e32 v50, 0xffff0000, v50
	v_add_f32_e32 v108, v108, v10
	v_add_f32_e32 v109, v109, v11
	v_mul_f32_e32 v108, v108, v17
	v_mul_f32_e32 v109, v109, v50
	v_cvt_pk_bf16_f32 v50, v108, v109
	s_nop 1
	v_permlane16_swap_b32_e32 v50, v51
	v_permlane16_swap_b32_e32 v52, v53
	s_nop 1
	v_permlane32_swap_b32_e32 v50, v52
	v_permlane32_swap_b32_e32 v51, v53
	global_store_dwordx4 v232, v[50:53], s[80:81]
	v_add_u32_e32 v232, 0xffffe000, v232
	global_load_dwordx4 v[42:45], v231, s[82:83] nt
	global_load_dwordx4 v[46:49], v231, s[84:85] nt
	global_load_dwordx4 v[50:53], v231, s[78:79] nt
	v_add_u32_e32 v231, 0xffffe000, v231
	s_waitcnt vmcnt(12)
; __device__ __forceinline__ unsigned cvt_pk_bf16(float lo, float hi) { unsigned r; asm("v_cvt_pk_bf16_f32 %0, %1, %2" : "=v"(r) : "v"(lo), "v"(hi)); return r; }
; __device__ __forceinline__ float bf_lo(unsigned w) { return __uint_as_float(w << 16); }
; __device__ __forceinline__ float bf_hi(unsigned w) { return __uint_as_float(w & 0xffff0000u); }
; __device__ __forceinline__ void scan_s3(CTXA) {
;     ...
;         for (int g = 0; g < 4; ++g) { unsigned wl[16], wb[16], wg[16];
; #pragma unroll
;             for (int q = 0; q < 16; ++q) { const int t = 63 - (g * 16 + q); wl[q] = __builtin_nontemporal_load(la1 + (size_t)t * (D / 2)); wb[q] = __builtin_nontemporal_load(bb1 + (size_t)t * (D / 2)); wg[q] = __builtin_nontemporal_load(gg + (size_t)t * (D / 2)); }
; #pragma unroll
;             for (int q = 0; q < 16; ++q) { const int t = 63 - (g * 16 + q); hb0 = __expf(bf_lo(wl[q])) * hb0 + bf_lo(wb[q]); hb1 = __expf(bf_hi(wl[q])) * hb1 + bf_hi(wb[q]);
;                 yy[(size_t)t * (D / 2)] = cvt_pk_bf16((fv0[t] + hb0) * bf_lo(wg[q]), (fv1[t] + hb1) * bf_hi(wg[q])); } }
	v_permlane16_swap_b32_e32 v54, v55
	v_permlane16_swap_b32_e32 v56, v57
	v_permlane16_swap_b32_e32 v58, v59
	v_permlane16_swap_b32_e32 v60, v61
	v_permlane16_swap_b32_e32 v62, v63
	v_permlane16_swap_b32_e32 v64, v65
	v_permlane32_swap_b32_e32 v54, v56
	v_permlane32_swap_b32_e32 v55, v57
	v_permlane32_swap_b32_e32 v58, v60
	v_permlane32_swap_b32_e32 v59, v61
	v_permlane32_swap_b32_e32 v62, v64
	v_permlane32_swap_b32_e32 v63, v65
	v_and_b32_e32 v6, 0xffff0000, v54
	v_lshlrev_b32_e32 v54, 16, v54
	v_and_b32_e32 v7, 0xffff0000, v55
	v_lshlrev_b32_e32 v55, 16, v55
	v_and_b32_e32 v14, 0xffff0000, v56
	v_lshlrev_b32_e32 v56, 16, v56
	v_and_b32_e32 v15, 0xffff0000, v57
	v_lshlrev_b32_e32 v57, 16, v57
	v_mul_f32_e32 v54, 0x3fb8aa3b, v54
	v_mul_f32_e32 v6, 0x3fb8aa3b, v6
	v_mul_f32_e32 v55, 0x3fb8aa3b, v55
	v_mul_f32_e32 v7, 0x3fb8aa3b, v7
	v_mul_f32_e32 v56, 0x3fb8aa3b, v56
	v_mul_f32_e32 v14, 0x3fb8aa3b, v14
	v_mul_f32_e32 v57, 0x3fb8aa3b, v57
	v_mul_f32_e32 v15, 0x3fb8aa3b, v15
	v_exp_f32_e32 v54, v54
	v_exp_f32_e32 v6, v6
	v_exp_f32_e32 v55, v55
	v_exp_f32_e32 v7, v7
	v_exp_f32_e32 v56, v56
	v_exp_f32_e32 v14, v14
	v_exp_f32_e32 v57, v57
	v_exp_f32_e32 v15, v15
	v_lshlrev_b32_e32 v12, 16, v61
	v_and_b32_e32 v13, 0xffff0000, v61
	v_fmac_f32_e32 v12, v10, v57
	v_fmac_f32_e32 v13, v11, v15
	v_lshlrev_b32_e32 v17, 16, v65
	v_and_b32_e32 v65, 0xffff0000, v65
	v_add_f32_e32 v106, v106, v12
	v_add_f32_e32 v107, v107, v13
	v_mul_f32_e32 v106, v106, v17
	v_mul_f32_e32 v107, v107, v65
	v_cvt_pk_bf16_f32 v65, v106, v107
	v_lshlrev_b32_e32 v10, 16, v60
	v_and_b32_e32 v11, 0xffff0000, v60
	v_fmac_f32_e32 v10, v12, v56
	v_fmac_f32_e32 v11, v13, v14
	v_lshlrev_b32_e32 v17, 16, v64
	v_and_b32_e32 v64, 0xffff0000, v64
	v_add_f32_e32 v104, v104, v10
	v_add_f32_e32 v105, v105, v11
	v_mul_f32_e32 v104, v104, v17
	v_mul_f32_e32 v105, v105, v64
	v_cvt_pk_bf16_f32 v64, v104, v105
	v_lshlrev_b32_e32 v12, 16, v59
	v_and_b32_e32 v13, 0xffff0000, v59
	v_fmac_f32_e32 v12, v10, v55
	v_fmac_f32_e32 v13, v11, v7
	v_lshlrev_b32_e32 v17, 16, v63
	v_and_b32_e32 v63, 0xffff0000, v63
	v_add_f32_e32 v102, v102, v12
	v_add_f32_e32 v103, v103, v13
	v_mul_f32_e32 v102, v102, v17
	v_mul_f32_e32 v103, v103, v63
	v_cvt_pk_bf16_f32 v63, v102, v103
	v_lshlrev_b32_e32 v10, 16, v58
	v_and_b32_e32 v11, 0xffff0000, v58
	v_fmac_f32_e32 v10, v12, v54
	v_fmac_f32_e32 v11, v13, v6
	v_lshlrev_b32_e32 v17, 16, v62
	v_and_b32_e32 v62, 0xffff0000, v62
	v_add_f32_e32 v100, v100, v10
	v_add_f32_e32 v101, v101, v11
	v_mul_f32_e32 v100, v100, v17
	v_mul_f32_e32 v101, v101, v62
	v_cvt_pk_bf16_f32 v62, v100, v101
	s_nop 1
	v_permlane16_swap_b32_e32 v62, v63
	v_permlane16_swap_b32_e32 v64, v65
	s_nop 1
	v_permlane32_swap_b32_e32 v62, v64
	v_permlane32_swap_b32_e32 v63, v65
	global_store_dwordx4 v232, v[62:65], s[80:81]
	v_add_u32_e32 v232, 0xffffe000, v232
	global_load_dwordx4 v[54:57], v231, s[82:83] nt
	global_load_dwordx4 v[58:61], v231, s[84:85] nt
	global_load_dwordx4 v[62:65], v231, s[78:79] nt
	s_waitcnt vmcnt(12)
	v_permlane16_swap_b32_e32 v18, v19
	v_permlane16_swap_b32_e32 v20, v21
	v_permlane16_swap_b32_e32 v22, v23
	v_permlane16_swap_b32_e32 v24, v25
	v_permlane16_swap_b32_e32 v26, v27
	v_permlane16_swap_b32_e32 v28, v29
	v_permlane32_swap_b32_e32 v18, v20
	v_permlane32_swap_b32_e32 v19, v21
	v_permlane32_swap_b32_e32 v22, v24
	v_permlane32_swap_b32_e32 v23, v25
	v_permlane32_swap_b32_e32 v26, v28
	v_permlane32_swap_b32_e32 v27, v29
	v_and_b32_e32 v6, 0xffff0000, v18
	v_lshlrev_b32_e32 v18, 16, v18
	v_and_b32_e32 v7, 0xffff0000, v19
	v_lshlrev_b32_e32 v19, 16, v19
	v_and_b32_e32 v14, 0xffff0000, v20
	v_lshlrev_b32_e32 v20, 16, v20
	v_and_b32_e32 v15, 0xffff0000, v21
	v_lshlrev_b32_e32 v21, 16, v21
	v_mul_f32_e32 v18, 0x3fb8aa3b, v18
	v_mul_f32_e32 v6, 0x3fb8aa3b, v6
	v_mul_f32_e32 v19, 0x3fb8aa3b, v19
	v_mul_f32_e32 v7, 0x3fb8aa3b, v7
	v_mul_f32_e32 v20, 0x3fb8aa3b, v20
	v_mul_f32_e32 v14, 0x3fb8aa3b, v14
	v_mul_f32_e32 v21, 0x3fb8aa3b, v21
	v_mul_f32_e32 v15, 0x3fb8aa3b, v15
	v_exp_f32_e32 v18, v18
	v_exp_f32_e32 v6, v6
	v_exp_f32_e32 v19, v19
	v_exp_f32_e32 v7, v7
	v_exp_f32_e32 v20, v20
	v_exp_f32_e32 v14, v14
	v_exp_f32_e32 v21, v21
	v_exp_f32_e32 v15, v15
	v_lshlrev_b32_e32 v12, 16, v25
	v_and_b32_e32 v13, 0xffff0000, v25
	v_fmac_f32_e32 v12, v10, v21
	v_fmac_f32_e32 v13, v11, v15
	v_lshlrev_b32_e32 v17, 16, v29
	v_and_b32_e32 v29, 0xffff0000, v29
	v_add_f32_e32 v98, v98, v12
	v_add_f32_e32 v99, v99, v13
	v_mul_f32_e32 v98, v98, v17
	v_mul_f32_e32 v99, v99, v29
	v_cvt_pk_bf16_f32 v29, v98, v99
	v_lshlrev_b32_e32 v10, 16, v24
	v_and_b32_e32 v11, 0xffff0000, v24
	v_fmac_f32_e32 v10, v12, v20
	v_fmac_f32_e32 v11, v13, v14
	v_lshlrev_b32_e32 v17, 16, v28
	v_and_b32_e32 v28, 0xffff0000, v28
	v_add_f32_e32 v96, v96, v10
	v_add_f32_e32 v97, v97, v11
	v_mul_f32_e32 v96, v96, v17
	v_mul_f32_e32 v97, v97, v28
	v_cvt_pk_bf16_f32 v28, v96, v97
	v_lshlrev_b32_e32 v12, 16, v23
	v_and_b32_e32 v13, 0xffff0000, v23
	v_fmac_f32_e32 v12, v10, v19
	v_fmac_f32_e32 v13, v11, v7
	v_lshlrev_b32_e32 v17, 16, v27
	v_and_b32_e32 v27, 0xffff0000, v27
	v_add_f32_e32 v94, v94, v12
	v_add_f32_e32 v95, v95, v13
	v_mul_f32_e32 v94, v94, v17
	v_mul_f32_e32 v95, v95, v27
	v_cvt_pk_bf16_f32 v27, v94, v95
	v_lshlrev_b32_e32 v10, 16, v22
	v_and_b32_e32 v11, 0xffff0000, v22
	v_fmac_f32_e32 v10, v12, v18
	v_fmac_f32_e32 v11, v13, v6
	v_lshlrev_b32_e32 v17, 16, v26
	v_and_b32_e32 v26, 0xffff0000, v26
	v_add_f32_e32 v92, v92, v10
	v_add_f32_e32 v93, v93, v11
	v_mul_f32_e32 v92, v92, v17
	v_mul_f32_e32 v93, v93, v26
	v_cvt_pk_bf16_f32 v26, v92, v93
	s_nop 1
	v_permlane16_swap_b32_e32 v26, v27
	v_permlane16_swap_b32_e32 v28, v29
	s_nop 1
	v_permlane32_swap_b32_e32 v26, v28
	v_permlane32_swap_b32_e32 v27, v29
	global_store_dwordx4 v232, v[26:29], s[80:81]
	v_add_u32_e32 v232, 0xffffe000, v232
	s_waitcnt vmcnt(9)
; __device__ __forceinline__ unsigned cvt_pk_bf16(float lo, float hi) { unsigned r; asm("v_cvt_pk_bf16_f32 %0, %1, %2" : "=v"(r) : "v"(lo), "v"(hi)); return r; }
; __device__ __forceinline__ float bf_lo(unsigned w) { return __uint_as_float(w << 16); }
; __device__ __forceinline__ float bf_hi(unsigned w) { return __uint_as_float(w & 0xffff0000u); }
; __device__ __forceinline__ void scan_s3(CTXA) {
;     ...
;         for (int g = 0; g < 4; ++g) { unsigned wl[16], wb[16], wg[16];
; #pragma unroll
;             for (int q = 0; q < 16; ++q) { const int t = 63 - (g * 16 + q); wl[q] = __builtin_nontemporal_load(la1 + (size_t)t * (D / 2)); wb[q] = __builtin_nontemporal_load(bb1 + (size_t)t * (D / 2)); wg[q] = __builtin_nontemporal_load(gg + (size_t)t * (D / 2)); }
; #pragma unroll
;             for (int q = 0; q < 16; ++q) { const int t = 63 - (g * 16 + q); hb0 = __expf(bf_lo(wl[q])) * hb0 + bf_lo(wb[q]); hb1 = __expf(bf_hi(wl[q])) * hb1 + bf_hi(wb[q]);
;                 yy[(size_t)t * (D / 2)] = cvt_pk_bf16((fv0[t] + hb0) * bf_lo(wg[q]), (fv1[t] + hb1) * bf_hi(wg[q])); } }
	v_permlane16_swap_b32_e32 v30, v31
	v_permlane16_swap_b32_e32 v32, v33
	v_permlane16_swap_b32_e32 v34, v35
	v_permlane16_swap_b32_e32 v36, v37
	v_permlane16_swap_b32_e32 v38, v39
	v_permlane16_swap_b32_e32 v40, v41
	v_permlane32_swap_b32_e32 v30, v32
	v_permlane32_swap_b32_e32 v31, v33
	v_permlane32_swap_b32_e32 v34, v36
	v_permlane32_swap_b32_e32 v35, v37
	v_permlane32_swap_b32_e32 v38, v40
	v_permlane32_swap_b32_e32 v39, v41
	v_and_b32_e32 v6, 0xffff0000, v30
	v_lshlrev_b32_e32 v30, 16, v30
	v_and_b32_e32 v7, 0xffff0000, v31
	v_lshlrev_b32_e32 v31, 16, v31
	v_and_b32_e32 v14, 0xffff0000, v32
	v_lshlrev_b32_e32 v32, 16, v32
	v_and_b32_e32 v15, 0xffff0000, v33
	v_lshlrev_b32_e32 v33, 16, v33
	v_mul_f32_e32 v30, 0x3fb8aa3b, v30
	v_mul_f32_e32 v6, 0x3fb8aa3b, v6
	v_mul_f32_e32 v31, 0x3fb8aa3b, v31
	v_mul_f32_e32 v7, 0x3fb8aa3b, v7
	v_mul_f32_e32 v32, 0x3fb8aa3b, v32
	v_mul_f32_e32 v14, 0x3fb8aa3b, v14
	v_mul_f32_e32 v33, 0x3fb8aa3b, v33
	v_mul_f32_e32 v15, 0x3fb8aa3b, v15
	v_exp_f32_e32 v30, v30
	v_exp_f32_e32 v6, v6
	v_exp_f32_e32 v31, v31
	v_exp_f32_e32 v7, v7
	v_exp_f32_e32 v32, v32
	v_exp_f32_e32 v14, v14
	v_exp_f32_e32 v33, v33
	v_exp_f32_e32 v15, v15
	v_lshlrev_b32_e32 v12, 16, v37
	v_and_b32_e32 v13, 0xffff0000, v37
	v_fmac_f32_e32 v12, v10, v33
	v_fmac_f32_e32 v13, v11, v15
	v_lshlrev_b32_e32 v17, 16, v41
	v_and_b32_e32 v41, 0xffff0000, v41
	v_add_f32_e32 v90, v90, v12
	v_add_f32_e32 v91, v91, v13
	v_mul_f32_e32 v90, v90, v17
	v_mul_f32_e32 v91, v91, v41
	v_cvt_pk_bf16_f32 v41, v90, v91
	v_lshlrev_b32_e32 v10, 16, v36
	v_and_b32_e32 v11, 0xffff0000, v36
	v_fmac_f32_e32 v10, v12, v32
	v_fmac_f32_e32 v11, v13, v14
	v_lshlrev_b32_e32 v17, 16, v40
	v_and_b32_e32 v40, 0xffff0000, v40
	v_add_f32_e32 v88, v88, v10
	v_add_f32_e32 v89, v89, v11
	v_mul_f32_e32 v88, v88, v17
	v_mul_f32_e32 v89, v89, v40
	v_cvt_pk_bf16_f32 v40, v88, v89
	v_lshlrev_b32_e32 v12, 16, v35
	v_and_b32_e32 v13, 0xffff0000, v35
	v_fmac_f32_e32 v12, v10, v31
	v_fmac_f32_e32 v13, v11, v7
	v_lshlrev_b32_e32 v17, 16, v39
	v_and_b32_e32 v39, 0xffff0000, v39
	v_add_f32_e32 v86, v86, v12
	v_add_f32_e32 v87, v87, v13
	v_mul_f32_e32 v86, v86, v17
	v_mul_f32_e32 v87, v87, v39
	v_cvt_pk_bf16_f32 v39, v86, v87
	v_lshlrev_b32_e32 v10, 16, v34
	v_and_b32_e32 v11, 0xffff0000, v34
	v_fmac_f32_e32 v10, v12, v30
	v_fmac_f32_e32 v11, v13, v6
	v_lshlrev_b32_e32 v17, 16, v38
	v_and_b32_e32 v38, 0xffff0000, v38
	v_add_f32_e32 v84, v84, v10
	v_add_f32_e32 v85, v85, v11
	v_mul_f32_e32 v84, v84, v17
	v_mul_f32_e32 v85, v85, v38
	v_cvt_pk_bf16_f32 v38, v84, v85
	s_nop 1
	v_permlane16_swap_b32_e32 v38, v39
	v_permlane16_swap_b32_e32 v40, v41
	s_nop 1
	v_permlane32_swap_b32_e32 v38, v40
	v_permlane32_swap_b32_e32 v39, v41
	global_store_dwordx4 v232, v[38:41], s[80:81]
	v_add_u32_e32 v232, 0xffffe000, v232
	s_waitcnt vmcnt(6)
	v_permlane16_swap_b32_e32 v42, v43
	v_permlane16_swap_b32_e32 v44, v45
	v_permlane16_swap_b32_e32 v46, v47
	v_permlane16_swap_b32_e32 v48, v49
	v_permlane16_swap_b32_e32 v50, v51
	v_permlane16_swap_b32_e32 v52, v53
	v_permlane32_swap_b32_e32 v42, v44
	v_permlane32_swap_b32_e32 v43, v45
	v_permlane32_swap_b32_e32 v46, v48
	v_permlane32_swap_b32_e32 v47, v49
	v_permlane32_swap_b32_e32 v50, v52
	v_permlane32_swap_b32_e32 v51, v53
	v_and_b32_e32 v6, 0xffff0000, v42
	v_lshlrev_b32_e32 v42, 16, v42
	v_and_b32_e32 v7, 0xffff0000, v43
	v_lshlrev_b32_e32 v43, 16, v43
	v_and_b32_e32 v14, 0xffff0000, v44
	v_lshlrev_b32_e32 v44, 16, v44
	v_and_b32_e32 v15, 0xffff0000, v45
	v_lshlrev_b32_e32 v45, 16, v45
	v_mul_f32_e32 v42, 0x3fb8aa3b, v42
	v_mul_f32_e32 v6, 0x3fb8aa3b, v6
	v_mul_f32_e32 v43, 0x3fb8aa3b, v43
	v_mul_f32_e32 v7, 0x3fb8aa3b, v7
	v_mul_f32_e32 v44, 0x3fb8aa3b, v44
	v_mul_f32_e32 v14, 0x3fb8aa3b, v14
	v_mul_f32_e32 v45, 0x3fb8aa3b, v45
	v_mul_f32_e32 v15, 0x3fb8aa3b, v15
	v_exp_f32_e32 v42, v42
	v_exp_f32_e32 v6, v6
	v_exp_f32_e32 v43, v43
	v_exp_f32_e32 v7, v7
	v_exp_f32_e32 v44, v44
	v_exp_f32_e32 v14, v14
	v_exp_f32_e32 v45, v45
	v_exp_f32_e32 v15, v15
	v_lshlrev_b32_e32 v12, 16, v49
	v_and_b32_e32 v13, 0xffff0000, v49
	v_fmac_f32_e32 v12, v10, v45
	v_fmac_f32_e32 v13, v11, v15
	v_lshlrev_b32_e32 v17, 16, v53
	v_and_b32_e32 v53, 0xffff0000, v53
	v_add_f32_e32 v82, v82, v12
	v_add_f32_e32 v83, v83, v13
	v_mul_f32_e32 v82, v82, v17
	v_mul_f32_e32 v83, v83, v53
	v_cvt_pk_bf16_f32 v53, v82, v83
	v_lshlrev_b32_e32 v10, 16, v48
	v_and_b32_e32 v11, 0xffff0000, v48
	v_fmac_f32_e32 v10, v12, v44
	v_fmac_f32_e32 v11, v13, v14
	v_lshlrev_b32_e32 v17, 16, v52
	v_and_b32_e32 v52, 0xffff0000, v52
	v_add_f32_e32 v80, v80, v10
	v_add_f32_e32 v81, v81, v11
	v_mul_f32_e32 v80, v80, v17
	v_mul_f32_e32 v81, v81, v52
	v_cvt_pk_bf16_f32 v52, v80, v81
	v_lshlrev_b32_e32 v12, 16, v47
	v_and_b32_e32 v13, 0xffff0000, v47
	v_fmac_f32_e32 v12, v10, v43
	v_fmac_f32_e32 v13, v11, v7
	v_lshlrev_b32_e32 v17, 16, v51
	v_and_b32_e32 v51, 0xffff0000, v51
	v_add_f32_e32 v78, v78, v12
	v_add_f32_e32 v79, v79, v13
	v_mul_f32_e32 v78, v78, v17
	v_mul_f32_e32 v79, v79, v51
	v_cvt_pk_bf16_f32 v51, v78, v79
	v_lshlrev_b32_e32 v10, 16, v46
	v_and_b32_e32 v11, 0xffff0000, v46
	v_fmac_f32_e32 v10, v12, v42
	v_fmac_f32_e32 v11, v13, v6
	v_lshlrev_b32_e32 v17, 16, v50
	v_and_b32_e32 v50, 0xffff0000, v50
	v_add_f32_e32 v76, v76, v10
	v_add_f32_e32 v77, v77, v11
	v_mul_f32_e32 v76, v76, v17
	v_mul_f32_e32 v77, v77, v50
	v_cvt_pk_bf16_f32 v50, v76, v77
	s_nop 1
	v_permlane16_swap_b32_e32 v50, v51
	v_permlane16_swap_b32_e32 v52, v53
	s_nop 1
	v_permlane32_swap_b32_e32 v50, v52
	v_permlane32_swap_b32_e32 v51, v53
	global_store_dwordx4 v232, v[50:53], s[80:81]
	v_add_u32_e32 v232, 0xffffe000, v232
	s_waitcnt vmcnt(3)
; __device__ __forceinline__ void scan_s3(CTXA) {
;     ...
;     for (int it = F.gw; it < NB * 64 * 8; it += F.NGW) {
;         const int cg = it & 7, chunk = (it >> 3) & 63, b = it >> 9;
;         const int ch = cg * 128 + 2 * F.lane;
;         float hf0 = 0.f, hf1 = 0.f, hb0 = 0.f, hb1 = 0.f;
;         for (int c0 = 0; c0 < chunk; c0 += 16) { f32x2 av[16], bv[16];
; #pragma unroll
;             for (int q = 0; q < 16; ++q) { const int c = c0 + q; const bool ok = c < chunk; const size_t o = ((size_t)((0 * NB + b) * 64 + (ok ? c : 0))) * D + ch;
;                 av[q] = *(const f32x2*)(CA + o); bv[q] = *(const f32x2*)(CB + o); if (!ok) { av[q] = (f32x2){0.f, 0.f}; bv[q] = (f32x2){0.f, 0.f}; } }
; #pragma unroll
;             for (int q = 0; q < 16; ++q) { hf0 = __expf(av[q].x) * hf0 + bv[q].x; hf1 = __expf(av[q].y) * hf1 + bv[q].y; } }
;         for (int c0 = 63; c0 > chunk; c0 -= 16) { f32x2 av[16], bv[16];
; #pragma unroll
;             for (int q = 0; q < 16; ++q) { const int c = c0 - q; const bool ok = c > chunk; const size_t o = ((size_t)((1 * NB + b) * 64 + (ok ? c : 63))) * D + ch;
;                 av[q] = *(const f32x2*)(CA + o); bv[q] = *(const f32x2*)(CB + o); if (!ok) { av[q] = (f32x2){0.f, 0.f}; bv[q] = (f32x2){0.f, 0.f}; } }
; #pragma unroll
;             for (int q = 0; q < 16; ++q) { hb0 = __expf(av[q].x) * hb0 + bv[q].x; hb1 = __expf(av[q].y) * hb1 + bv[q].y; } }
;         const size_t e0 = ((size_t)b * S + chunk * 64) * D + ch;
;         const unsigned* la0 = (const unsigned*)(LA + e0); const unsigned* bb0 = (const unsigned*)(BB + e0);
;         const unsigned* la1 = (const unsigned*)(LA + (size_t)T * D + e0); const unsigned* bb1 = (const unsigned*)(BB + (size_t)T * D + e0);
;     ...
;         for (int g = 0; g < 4; ++g) { unsigned wl[16], wb[16], wg[16];
; #pragma unroll
;             for (int q = 0; q < 16; ++q) { const int t = 63 - (g * 16 + q); wl[q] = __builtin_nontemporal_load(la1 + (size_t)t * (D / 2)); wb[q] = __builtin_nontemporal_load(bb1 + (size_t)t * (D / 2)); wg[q] = __builtin_nontemporal_load(gg + (size_t)t * (D / 2)); }
; #pragma unroll
;             for (int q = 0; q < 16; ++q) { const int t = 63 - (g * 16 + q); hb0 = __expf(bf_lo(wl[q])) * hb0 + bf_lo(wb[q]); hb1 = __expf(bf_hi(wl[q])) * hb1 + bf_hi(wb[q]);
;                 yy[(size_t)t * (D / 2)] = cvt_pk_bf16((fv0[t] + hb0) * bf_lo(wg[q]), (fv1[t] + hb1) * bf_hi(wg[q])); } }
	v_permlane16_swap_b32_e32 v54, v55
	v_permlane16_swap_b32_e32 v56, v57
	v_permlane16_swap_b32_e32 v58, v59
	v_permlane16_swap_b32_e32 v60, v61
	v_permlane16_swap_b32_e32 v62, v63
	v_permlane16_swap_b32_e32 v64, v65
	v_permlane32_swap_b32_e32 v54, v56
	v_permlane32_swap_b32_e32 v55, v57
	v_permlane32_swap_b32_e32 v58, v60
	v_permlane32_swap_b32_e32 v59, v61
	v_permlane32_swap_b32_e32 v62, v64
	v_permlane32_swap_b32_e32 v63, v65
	v_and_b32_e32 v6, 0xffff0000, v54
	v_lshlrev_b32_e32 v54, 16, v54
	v_and_b32_e32 v7, 0xffff0000, v55
	v_lshlrev_b32_e32 v55, 16, v55
	v_and_b32_e32 v14, 0xffff0000, v56
	v_lshlrev_b32_e32 v56, 16, v56
	v_and_b32_e32 v15, 0xffff0000, v57
	v_lshlrev_b32_e32 v57, 16, v57
	v_mul_f32_e32 v54, 0x3fb8aa3b, v54
	v_mul_f32_e32 v6, 0x3fb8aa3b, v6
	v_mul_f32_e32 v55, 0x3fb8aa3b, v55
	v_mul_f32_e32 v7, 0x3fb8aa3b, v7
	v_mul_f32_e32 v56, 0x3fb8aa3b, v56
	v_mul_f32_e32 v14, 0x3fb8aa3b, v14
	v_mul_f32_e32 v57, 0x3fb8aa3b, v57
	v_mul_f32_e32 v15, 0x3fb8aa3b, v15
	v_exp_f32_e32 v54, v54
	v_exp_f32_e32 v6, v6
	v_exp_f32_e32 v55, v55
	v_exp_f32_e32 v7, v7
	v_exp_f32_e32 v56, v56
	v_exp_f32_e32 v14, v14
	v_exp_f32_e32 v57, v57
	v_exp_f32_e32 v15, v15
	v_lshlrev_b32_e32 v12, 16, v61
	v_and_b32_e32 v13, 0xffff0000, v61
	v_fmac_f32_e32 v12, v10, v57
	v_fmac_f32_e32 v13, v11, v15
	v_lshlrev_b32_e32 v17, 16, v65
	v_and_b32_e32 v65, 0xffff0000, v65
	v_add_f32_e32 v74, v74, v12
	v_add_f32_e32 v75, v75, v13
	v_mul_f32_e32 v74, v74, v17
	v_mul_f32_e32 v75, v75, v65
	v_cvt_pk_bf16_f32 v65, v74, v75
	v_lshlrev_b32_e32 v10, 16, v60
	v_and_b32_e32 v11, 0xffff0000, v60
	v_fmac_f32_e32 v10, v12, v56
	v_fmac_f32_e32 v11, v13, v14
	v_lshlrev_b32_e32 v17, 16, v64
	v_and_b32_e32 v64, 0xffff0000, v64
	v_add_f32_e32 v72, v72, v10
	v_add_f32_e32 v73, v73, v11
	v_mul_f32_e32 v72, v72, v17
	v_mul_f32_e32 v73, v73, v64
	v_cvt_pk_bf16_f32 v64, v72, v73
	v_lshlrev_b32_e32 v12, 16, v59
	v_and_b32_e32 v13, 0xffff0000, v59
	v_fmac_f32_e32 v12, v10, v55
	v_fmac_f32_e32 v13, v11, v7
	v_lshlrev_b32_e32 v17, 16, v63
	v_and_b32_e32 v63, 0xffff0000, v63
	v_add_f32_e32 v70, v70, v12
	v_add_f32_e32 v71, v71, v13
	v_mul_f32_e32 v70, v70, v17
	v_mul_f32_e32 v71, v71, v63
	v_cvt_pk_bf16_f32 v63, v70, v71
	v_lshlrev_b32_e32 v10, 16, v58
	v_and_b32_e32 v11, 0xffff0000, v58
	v_fmac_f32_e32 v10, v12, v54
	v_fmac_f32_e32 v11, v13, v6
	v_lshlrev_b32_e32 v17, 16, v62
	v_and_b32_e32 v62, 0xffff0000, v62
	v_add_f32_e32 v68, v68, v10
	v_add_f32_e32 v69, v69, v11
	v_mul_f32_e32 v68, v68, v17
	v_mul_f32_e32 v69, v69, v62
	v_cvt_pk_bf16_f32 v62, v68, v69
	s_nop 1
	v_permlane16_swap_b32_e32 v62, v63
	v_permlane16_swap_b32_e32 v64, v65
	s_nop 1
	v_permlane32_swap_b32_e32 v62, v64
	v_permlane32_swap_b32_e32 v63, v65
	global_store_dwordx4 v232, v[62:65], s[80:81]
	s_add_i32 s1, s1, s2
	s_add_i32 s12, s12, s13
	s_cmpk_gt_i32 s1, 0x7ff
	s_cbranch_scc1 .LBB0_184
.LBB0_174:
	s_lshl_b32 s0, s12, 2
	s_and_b32 s0, s0, 0xe00
	s_lshl_b32 s6, s1, 7
	v_lshl_or_b32 v66, v16, 2, s0
	s_bfe_u32 s0, s1, 0x60003
	s_ashr_i32 s10, s1, 9
	s_and_b32 s6, s6, 0x380
	v_or_b32_e32 v2, s6, v16
	s_lshl_b32 s7, s10, 22
	s_lshl_b32 s11, s0, 16
	s_or_b32 s7, s7, s11
	v_bfe_u32 v231, v2, 1, 2
	v_and_b32_e32 v232, 0xfffffff9, v2
	v_or_b32_e32 v230, s7, v232
	v_lshlrev_b32_e32 v230, 1, v230
	v_lshl_add_u32 v230, v231, 11, v230
	v_add_u32_e32 v231, 0x1e000, v230
	global_load_dwordx4 v[198:201], v230, s[70:71] nt
	global_load_dwordx4 v[202:205], v230, s[72:73] nt
	v_add_u32_e32 v230, 0x2000, v230
	global_load_dwordx4 v[206:209], v230, s[70:71] nt
	global_load_dwordx4 v[210:213], v230, s[72:73] nt
	v_add_u32_e32 v230, 0x2000, v230
	global_load_dwordx4 v[214:217], v230, s[70:71] nt
	global_load_dwordx4 v[218:221], v230, s[72:73] nt
	v_add_u32_e32 v230, 0x2000, v230
	global_load_dwordx4 v[222:225], v230, s[70:71] nt
	global_load_dwordx4 v[226:229], v230, s[72:73] nt
	v_add_u32_e32 v230, 0x2000, v230
	s_cmp_eq_u32 s0, 0
	s_cbranch_scc1 .LBB0_181
	s_lshl_b32 s16, s10, 6
	s_ashr_i32 s17, s16, 31
	s_lshl_b64 s[6:7], s[16:17], 12
	s_add_u32 s6, s8, s6
	s_addc_u32 s7, s9, s7
	v_mov_b32_e32 v8, 0
	v_lshl_add_u64 v[4:5], s[6:7], 0, v[66:67]
	s_mov_b32 s11, 0
	v_lshlrev_b32_e32 v1, 2, v2
	v_mov_b32_e32 v9, v8
